# int8 GEMM epilogues (in-projection, dense gate/up): the 8 per-row-group scale loads hoisted to the epilogue top; steps no longer wait on load+stores
# speedup vs baseline: 1.0284x; 1.0049x over previous
; __device__ __forceinline__ unsigned cvtpk(float lo, float hi) { f32x2 v = {lo, hi}; bf16x2_t b = __builtin_convertvector(v, bf16x2_t); return __builtin_bit_cast(unsigned, b); }
;     __device__ __forceinline__ void operator()(const f32x4 (&acc)[2][2][4][2], const Unit& u, int wr, int wc, int fr, int fq) const {
;         typedef int i32x4_ __attribute__((ext_vector_type(4)));
;         const int row0 = u.pm * BM + wr * 64 + fr, col0 = u.pn * BM + wc * 32 + 8 * fq;
;         const float qsc = (u.pn < 2 || (u.pn >= 14 && u.pn < 18)) ? 0.125f * 1.4426950408889634f : 1.f;
;         f32x4 cmv[2][2], cs[2][2];
; #pragma unroll
;         for (int bj = 0; bj < 2; ++bj)
; #pragma unroll
;             for (int n = 0; n < 2; ++n) { cmv[bj][n] = *(const f32x4*)(colmax + col0 + bj * HALF + 4 * n) * (qsc / (127.f * 127.f)); cs[bj][n] = (f32x4){0.f, 0.f, 0.f, 0.f}; }
; #pragma unroll
;         for (int ai = 0; ai < 2; ++ai)
; #pragma unroll
;             for (int m = 0; m < 4; ++m) { const int r = row0 + ai * HALF + m * 16; bf16_t* rowp = O + (size_t)r * ldc + col0; const float sa = rowmax[r];
; #pragma unroll
;                 for (int bj = 0; bj < 2; ++bj) { f32x4 v[2];
; #pragma unroll
;                     for (int n = 0; n < 2; ++n) { const i32x4_ iv = __builtin_bit_cast(i32x4_, acc[ai][bj][m][n]);
;                         v[n] = (f32x4){(float)iv[0], (float)iv[1], (float)iv[2], (float)iv[3]} * (cmv[bj][n] * sa); cs[bj][n] += v[n]; }
;                     u32x4 w; w.x = cvtpk(v[0][0], v[0][1]); w.y = cvtpk(v[0][2], v[0][3]); w.z = cvtpk(v[1][0], v[1][1]); w.w = cvtpk(v[1][2], v[1][3]);
;                     *(u32x4*)(rowp + bj * HALF) = w; } }
.LBB0_196:
	s_lshl_b32 s0, s31, 8
	v_or_b32_e32 v170, s0, v174
	v_ashrrev_i32_e32 v171, 31, v170
	v_lshl_add_u64 v[148:149], v[170:171], 2, s[16:17]
	global_load_dwordx4 v[154:157], v[148:149], off
	global_load_dwordx4 v[158:161], v[148:149], off offset:16
	global_load_dwordx4 v[166:169], v[148:149], off offset:528
	global_load_dwordx4 v[162:165], v[148:149], off offset:512
	v_lshl_add_u32 v148, s30, 8, v172
	v_ashrrev_i32_e32 v149, 31, v148
	v_lshl_add_u64 v[152:153], v[148:149], 2, s[14:15]
	global_load_dword v182, v[152:153], off
	global_load_dword v244, v[152:153], off offset:64
	global_load_dword v245, v[152:153], off offset:128
	global_load_dword v246, v[152:153], off offset:192
	global_load_dword v247, v[152:153], off offset:512
	global_load_dword v248, v[152:153], off offset:576
	global_load_dword v249, v[152:153], off offset:640
	global_load_dword v250, v[152:153], off offset:704
	v_mov_b64_e32 v[150:151], s[58:59]
	v_cvt_f32_i32_e32 v189, v117
	v_cvt_f32_i32_e32 v188, v116
	s_cmp_lt_i32 s31, 2
	v_mad_i64_i32 v[116:117], s[34:35], v148, s64, v[150:151]
	s_cselect_b64 s[34:35], -1, 0
	s_add_i32 s23, s31, -14
	s_cmp_lt_u32 s23, 4
	s_cselect_b64 s[36:37], -1, 0
	v_cvt_f32_i32_e32 v129, v129
	v_cvt_f32_i32_e32 v128, v128
	v_cvt_f32_i32_e32 v127, v127
	v_cvt_f32_i32_e32 v126, v126
	v_cvt_f32_i32_e32 v185, v125
	v_cvt_f32_i32_e32 v184, v124
	v_cvt_f32_i32_e32 v123, v123
	v_cvt_f32_i32_e32 v122, v122
	v_lshlrev_b64 v[170:171], 1, v[170:171]
	s_or_b64 vcc, s[34:35], s[36:37]
	v_cvt_f32_i32_e32 v187, v121
	v_cvt_f32_i32_e32 v186, v120
	v_cvt_f32_i32_e32 v119, v119
	v_cvt_f32_i32_e32 v118, v118
	v_cvt_f32_i32_e32 v115, v115
	v_cvt_f32_i32_e32 v114, v114
	v_lshl_add_u64 v[196:197], v[116:117], 0, v[170:171]
	v_cndmask_b32_e32 v116, v178, v179, vcc
	v_or_b32_e32 v190, 16, v148
	v_ashrrev_i32_e32 v191, 31, v190
	v_lshl_add_u64 v[192:193], v[190:191], 2, s[14:15]
	v_add_u32_e32 v1, 0x80, v148
	v_cvt_f32_i32_e32 v7, v7
	v_cvt_f32_i32_e32 v6, v6
	v_cvt_f32_i32_e32 v9, v9
	v_cvt_f32_i32_e32 v8, v8
	v_cvt_f32_i32_e32 v3, v3
	v_cvt_f32_i32_e32 v2, v2
	v_cvt_f32_i32_e32 v5, v5
	v_cvt_f32_i32_e32 v4, v4
	s_and_b32 s23, s31, -2
	s_cmp_lg_u32 s23, 2
	s_waitcnt vmcnt(0)
	v_pk_mul_f32 v[154:155], v[116:117], v[154:155] op_sel_hi:[0,1]
	v_pk_mul_f32 v[156:157], v[116:117], v[156:157] op_sel_hi:[0,1]
	v_pk_mul_f32 v[158:159], v[116:117], v[158:159] op_sel_hi:[0,1]
	v_pk_mul_f32 v[160:161], v[116:117], v[160:161] op_sel_hi:[0,1]
	v_pk_mul_f32 v[162:163], v[116:117], v[162:163] op_sel_hi:[0,1]
	v_pk_mul_f32 v[164:165], v[116:117], v[164:165] op_sel_hi:[0,1]
	v_pk_mul_f32 v[166:167], v[116:117], v[166:167] op_sel_hi:[0,1]
	v_pk_mul_f32 v[168:169], v[116:117], v[168:169] op_sel_hi:[0,1]
	v_pk_mul_f32 v[116:117], v[156:157], v[182:183] op_sel_hi:[1,0]
	v_pk_mul_f32 v[120:121], v[154:155], v[182:183] op_sel_hi:[1,0]
	v_pk_mul_f32 v[198:199], v[160:161], v[182:183] op_sel_hi:[1,0]
	v_pk_mul_f32 v[124:125], v[158:159], v[182:183] op_sel_hi:[1,0]
	v_pk_mul_f32 v[200:201], v[164:165], v[182:183] op_sel_hi:[1,0]
	v_pk_mul_f32 v[202:203], v[162:163], v[182:183] op_sel_hi:[1,0]
	v_pk_mul_f32 v[204:205], v[168:169], v[182:183] op_sel_hi:[1,0]
	v_pk_mul_f32 v[182:183], v[166:167], v[182:183] op_sel_hi:[1,0]
	v_pk_mul_f32 v[126:127], v[120:121], v[126:127]
	v_pk_mul_f32 v[128:129], v[116:117], v[128:129]
	v_pk_mul_f32 v[124:125], v[124:125], v[122:123]
	v_pk_mul_f32 v[122:123], v[198:199], v[184:185]
	v_pk_mul_f32 v[120:121], v[202:203], v[118:119]
	v_pk_mul_f32 v[118:119], v[200:201], v[186:187]
	v_pk_mul_f32 v[116:117], v[182:183], v[114:115]
	v_pk_mul_f32 v[114:115], v[204:205], v[188:189]
	v_cvt_pk_bf16_f32 v182, v126, v127
	v_cvt_pk_bf16_f32 v183, v128, v129
	v_cvt_pk_bf16_f32 v184, v124, v125
	v_cvt_pk_bf16_f32 v185, v122, v123
	v_cvt_pk_bf16_f32 v186, v120, v121
	v_cvt_pk_bf16_f32 v187, v118, v119
	v_cvt_pk_bf16_f32 v188, v116, v117
	v_cvt_pk_bf16_f32 v189, v114, v115
	global_store_dwordx4 v[196:197], v[182:185], off
	global_store_dwordx4 v[196:197], v[186:189], off offset:256
	s_nop 0
	v_mov_b32_e32 v182, v244
	v_cvt_f32_i32_e32 v185, v111
	v_cvt_f32_i32_e32 v184, v110
	v_cvt_f32_i32_e32 v111, v113
	v_cvt_f32_i32_e32 v110, v112
	v_cvt_f32_i32_e32 v187, v107
	v_cvt_f32_i32_e32 v186, v106
	v_cvt_f32_i32_e32 v107, v109
	v_cvt_f32_i32_e32 v106, v108
	v_cvt_f32_i32_e32 v189, v103
	v_cvt_f32_i32_e32 v188, v102
	v_cvt_f32_i32_e32 v103, v105
	v_cvt_f32_i32_e32 v102, v104
	v_cvt_f32_i32_e32 v193, v99
	v_cvt_f32_i32_e32 v192, v98
	v_cvt_f32_i32_e32 v99, v101
	v_cvt_f32_i32_e32 v98, v100
	v_mad_i64_i32 v[100:101], s[34:35], v190, s64, v[150:151]
	v_lshl_add_u64 v[198:199], v[100:101], 0, v[170:171]
	v_or_b32_e32 v196, 32, v148
	v_ashrrev_i32_e32 v197, 31, v196
	v_lshl_add_u64 v[190:191], v[196:197], 2, s[14:15]
	v_pk_mul_f32 v[100:101], v[154:155], v[182:183] op_sel_hi:[1,0]
	v_pk_mul_f32 v[104:105], v[156:157], v[182:183] op_sel_hi:[1,0]
	v_pk_mul_f32 v[108:109], v[158:159], v[182:183] op_sel_hi:[1,0]
	v_pk_mul_f32 v[200:201], v[160:161], v[182:183] op_sel_hi:[1,0]
	v_pk_mul_f32 v[202:203], v[162:163], v[182:183] op_sel_hi:[1,0]
	v_pk_mul_f32 v[204:205], v[164:165], v[182:183] op_sel_hi:[1,0]
	v_pk_mul_f32 v[206:207], v[166:167], v[182:183] op_sel_hi:[1,0]
	v_pk_mul_f32 v[182:183], v[168:169], v[182:183] op_sel_hi:[1,0]
	v_pk_mul_f32 v[110:111], v[104:105], v[110:111]
	v_pk_mul_f32 v[112:113], v[100:101], v[184:185]
	v_pk_mul_f32 v[106:107], v[200:201], v[106:107]
	v_pk_mul_f32 v[108:109], v[108:109], v[186:187]
	v_pk_mul_f32 v[102:103], v[204:205], v[102:103]
	v_pk_mul_f32 v[104:105], v[202:203], v[188:189]
	v_pk_mul_f32 v[98:99], v[182:183], v[98:99]
; __device__ __forceinline__ unsigned cvtpk(float lo, float hi) { f32x2 v = {lo, hi}; bf16x2_t b = __builtin_convertvector(v, bf16x2_t); return __builtin_bit_cast(unsigned, b); }
;     __device__ __forceinline__ void operator()(const f32x4 (&acc)[2][2][4][2], const Unit& u, int wr, int wc, int fr, int fq) const {
;     ...
;             for (int m = 0; m < 4; ++m) { const int r = row0 + ai * HALF + m * 16; bf16_t* rowp = O + (size_t)r * ldc + col0; const float sa = rowmax[r];
; #pragma unroll
;                 for (int bj = 0; bj < 2; ++bj) { f32x4 v[2];
; #pragma unroll
;                     for (int n = 0; n < 2; ++n) { const i32x4_ iv = __builtin_bit_cast(i32x4_, acc[ai][bj][m][n]);
;                         v[n] = (f32x4){(float)iv[0], (float)iv[1], (float)iv[2], (float)iv[3]} * (cmv[bj][n] * sa); cs[bj][n] += v[n]; }
;                     u32x4 w; w.x = cvtpk(v[0][0], v[0][1]); w.y = cvtpk(v[0][2], v[0][3]); w.z = cvtpk(v[1][0], v[1][1]); w.w = cvtpk(v[1][2], v[1][3]);
;                     *(u32x4*)(rowp + bj * HALF) = w; } }
	v_pk_mul_f32 v[100:101], v[206:207], v[192:193]
	v_cvt_pk_bf16_f32 v182, v112, v113
	v_cvt_pk_bf16_f32 v183, v110, v111
	v_cvt_pk_bf16_f32 v184, v108, v109
	v_cvt_pk_bf16_f32 v185, v106, v107
	v_cvt_pk_bf16_f32 v186, v104, v105
	v_cvt_pk_bf16_f32 v187, v102, v103
	v_cvt_pk_bf16_f32 v188, v100, v101
	v_cvt_pk_bf16_f32 v189, v98, v99
	global_store_dwordx4 v[198:199], v[182:185], off
	global_store_dwordx4 v[198:199], v[186:189], off offset:256
	s_nop 0
	v_mov_b32_e32 v182, v245
	v_cvt_f32_i32_e32 v185, v95
	v_cvt_f32_i32_e32 v184, v94
	v_cvt_f32_i32_e32 v95, v97
	v_cvt_f32_i32_e32 v94, v96
	v_cvt_f32_i32_e32 v187, v91
	v_cvt_f32_i32_e32 v186, v90
	v_cvt_f32_i32_e32 v91, v93
	v_cvt_f32_i32_e32 v90, v92
	v_cvt_f32_i32_e32 v189, v87
	v_cvt_f32_i32_e32 v188, v86
	v_cvt_f32_i32_e32 v87, v89
	v_cvt_f32_i32_e32 v86, v88
	v_cvt_f32_i32_e32 v191, v83
	v_cvt_f32_i32_e32 v190, v82
	v_cvt_f32_i32_e32 v83, v85
	v_cvt_f32_i32_e32 v82, v84
	v_mad_i64_i32 v[84:85], s[34:35], v196, s64, v[150:151]
	v_lshl_add_u64 v[198:199], v[84:85], 0, v[170:171]
	v_or_b32_e32 v192, 48, v148
	v_ashrrev_i32_e32 v193, 31, v192
	v_lshl_add_u64 v[196:197], v[192:193], 2, s[14:15]
	v_pk_mul_f32 v[84:85], v[154:155], v[182:183] op_sel_hi:[1,0]
	v_pk_mul_f32 v[88:89], v[156:157], v[182:183] op_sel_hi:[1,0]
	v_pk_mul_f32 v[92:93], v[158:159], v[182:183] op_sel_hi:[1,0]
	v_pk_mul_f32 v[200:201], v[160:161], v[182:183] op_sel_hi:[1,0]
	v_pk_mul_f32 v[202:203], v[162:163], v[182:183] op_sel_hi:[1,0]
	v_pk_mul_f32 v[204:205], v[164:165], v[182:183] op_sel_hi:[1,0]
	v_pk_mul_f32 v[206:207], v[166:167], v[182:183] op_sel_hi:[1,0]
	v_pk_mul_f32 v[182:183], v[168:169], v[182:183] op_sel_hi:[1,0]
	v_pk_mul_f32 v[94:95], v[88:89], v[94:95]
	v_pk_mul_f32 v[96:97], v[84:85], v[184:185]
	v_pk_mul_f32 v[90:91], v[200:201], v[90:91]
	v_pk_mul_f32 v[92:93], v[92:93], v[186:187]
	v_pk_mul_f32 v[86:87], v[204:205], v[86:87]
	v_pk_mul_f32 v[88:89], v[202:203], v[188:189]
	v_pk_mul_f32 v[82:83], v[182:183], v[82:83]
	v_pk_mul_f32 v[84:85], v[206:207], v[190:191]
	v_cvt_pk_bf16_f32 v182, v96, v97
	v_cvt_pk_bf16_f32 v183, v94, v95
	v_cvt_pk_bf16_f32 v184, v92, v93
	v_cvt_pk_bf16_f32 v185, v90, v91
	v_cvt_pk_bf16_f32 v186, v88, v89
	v_cvt_pk_bf16_f32 v187, v86, v87
	v_cvt_pk_bf16_f32 v188, v84, v85
	v_cvt_pk_bf16_f32 v189, v82, v83
	global_store_dwordx4 v[198:199], v[182:185], off
	global_store_dwordx4 v[198:199], v[186:189], off offset:256
	s_nop 0
	v_mov_b32_e32 v182, v246
	v_cvt_f32_i32_e32 v185, v79
	v_cvt_f32_i32_e32 v184, v78
	v_cvt_f32_i32_e32 v79, v81
	v_cvt_f32_i32_e32 v78, v80
	v_cvt_f32_i32_e32 v187, v75
	v_cvt_f32_i32_e32 v186, v74
	v_cvt_f32_i32_e32 v75, v77
	v_cvt_f32_i32_e32 v74, v76
	v_cvt_f32_i32_e32 v189, v71
	v_cvt_f32_i32_e32 v188, v70
	v_cvt_f32_i32_e32 v71, v73
	v_cvt_f32_i32_e32 v70, v72
	v_cvt_f32_i32_e32 v191, v67
	v_cvt_f32_i32_e32 v190, v66
	v_cvt_f32_i32_e32 v67, v69
	v_cvt_f32_i32_e32 v66, v68
	v_mad_i64_i32 v[68:69], s[34:35], v192, s64, v[150:151]
	v_lshl_add_u64 v[192:193], v[68:69], 0, v[170:171]
	v_pk_mul_f32 v[68:69], v[154:155], v[182:183] op_sel_hi:[1,0]
	v_pk_mul_f32 v[72:73], v[156:157], v[182:183] op_sel_hi:[1,0]
	v_pk_mul_f32 v[76:77], v[158:159], v[182:183] op_sel_hi:[1,0]
	v_pk_mul_f32 v[196:197], v[160:161], v[182:183] op_sel_hi:[1,0]
	v_pk_mul_f32 v[198:199], v[162:163], v[182:183] op_sel_hi:[1,0]
	v_pk_mul_f32 v[200:201], v[164:165], v[182:183] op_sel_hi:[1,0]
	v_pk_mul_f32 v[202:203], v[166:167], v[182:183] op_sel_hi:[1,0]
	v_pk_mul_f32 v[182:183], v[168:169], v[182:183] op_sel_hi:[1,0]
	v_pk_mul_f32 v[78:79], v[72:73], v[78:79]
	v_pk_mul_f32 v[80:81], v[68:69], v[184:185]
	v_pk_mul_f32 v[74:75], v[196:197], v[74:75]
	v_pk_mul_f32 v[76:77], v[76:77], v[186:187]
	v_pk_mul_f32 v[70:71], v[200:201], v[70:71]
	v_pk_mul_f32 v[72:73], v[198:199], v[188:189]
	v_pk_mul_f32 v[66:67], v[182:183], v[66:67]
	v_pk_mul_f32 v[68:69], v[202:203], v[190:191]
	v_cvt_pk_bf16_f32 v182, v80, v81
	v_cvt_pk_bf16_f32 v183, v78, v79
	v_cvt_pk_bf16_f32 v184, v76, v77
	v_cvt_pk_bf16_f32 v185, v74, v75
	v_cvt_pk_bf16_f32 v186, v72, v73
	v_cvt_pk_bf16_f32 v187, v70, v71
	v_cvt_pk_bf16_f32 v188, v68, v69
	v_cvt_pk_bf16_f32 v189, v66, v67
	global_store_dwordx4 v[192:193], v[182:185], off
	global_store_dwordx4 v[192:193], v[186:189], off offset:256
	s_nop 0
	v_mov_b32_e32 v182, v247
	v_cvt_f32_i32_e32 v185, v63
	v_cvt_f32_i32_e32 v184, v62
	v_cvt_f32_i32_e32 v63, v65
	v_cvt_f32_i32_e32 v62, v64
	v_cvt_f32_i32_e32 v187, v59
	v_cvt_f32_i32_e32 v186, v58
	v_cvt_f32_i32_e32 v59, v61
	v_cvt_f32_i32_e32 v58, v60
	v_cvt_f32_i32_e32 v189, v55
	v_cvt_f32_i32_e32 v188, v54
	v_cvt_f32_i32_e32 v55, v57
	v_cvt_f32_i32_e32 v54, v56
	v_cvt_f32_i32_e32 v191, v51
	v_cvt_f32_i32_e32 v190, v50
	v_cvt_f32_i32_e32 v51, v53
	v_cvt_f32_i32_e32 v50, v52
	v_mad_i64_i32 v[52:53], s[34:35], v1, s64, v[150:151]
	v_lshl_add_u64 v[192:193], v[52:53], 0, v[170:171]
	v_add_u32_e32 v1, 0x90, v148
	v_pk_mul_f32 v[52:53], v[154:155], v[182:183] op_sel_hi:[1,0]
	v_pk_mul_f32 v[56:57], v[156:157], v[182:183] op_sel_hi:[1,0]
	v_pk_mul_f32 v[60:61], v[158:159], v[182:183] op_sel_hi:[1,0]
	v_pk_mul_f32 v[196:197], v[160:161], v[182:183] op_sel_hi:[1,0]
	v_pk_mul_f32 v[198:199], v[162:163], v[182:183] op_sel_hi:[1,0]
	v_pk_mul_f32 v[200:201], v[164:165], v[182:183] op_sel_hi:[1,0]
	v_pk_mul_f32 v[202:203], v[166:167], v[182:183] op_sel_hi:[1,0]
	v_pk_mul_f32 v[182:183], v[168:169], v[182:183] op_sel_hi:[1,0]
	v_pk_mul_f32 v[62:63], v[56:57], v[62:63]
	v_pk_mul_f32 v[64:65], v[52:53], v[184:185]
	v_pk_mul_f32 v[58:59], v[196:197], v[58:59]
	v_pk_mul_f32 v[60:61], v[60:61], v[186:187]
	v_pk_mul_f32 v[54:55], v[200:201], v[54:55]
; __device__ __forceinline__ unsigned cvtpk(float lo, float hi) { f32x2 v = {lo, hi}; bf16x2_t b = __builtin_convertvector(v, bf16x2_t); return __builtin_bit_cast(unsigned, b); }
;     __device__ __forceinline__ void operator()(const f32x4 (&acc)[2][2][4][2], const Unit& u, int wr, int wc, int fr, int fq) const {
;     ...
;             for (int m = 0; m < 4; ++m) { const int r = row0 + ai * HALF + m * 16; bf16_t* rowp = O + (size_t)r * ldc + col0; const float sa = rowmax[r];
; #pragma unroll
;                 for (int bj = 0; bj < 2; ++bj) { f32x4 v[2];
; #pragma unroll
;                     for (int n = 0; n < 2; ++n) { const i32x4_ iv = __builtin_bit_cast(i32x4_, acc[ai][bj][m][n]);
;                         v[n] = (f32x4){(float)iv[0], (float)iv[1], (float)iv[2], (float)iv[3]} * (cmv[bj][n] * sa); cs[bj][n] += v[n]; }
;                     u32x4 w; w.x = cvtpk(v[0][0], v[0][1]); w.y = cvtpk(v[0][2], v[0][3]); w.z = cvtpk(v[1][0], v[1][1]); w.w = cvtpk(v[1][2], v[1][3]);
;                     *(u32x4*)(rowp + bj * HALF) = w; } }
	v_pk_mul_f32 v[56:57], v[198:199], v[188:189]
	v_pk_mul_f32 v[50:51], v[182:183], v[50:51]
	v_pk_mul_f32 v[52:53], v[202:203], v[190:191]
	v_cvt_pk_bf16_f32 v182, v64, v65
	v_cvt_pk_bf16_f32 v183, v62, v63
	v_cvt_pk_bf16_f32 v184, v60, v61
	v_cvt_pk_bf16_f32 v185, v58, v59
	v_cvt_pk_bf16_f32 v186, v56, v57
	v_cvt_pk_bf16_f32 v187, v54, v55
	v_cvt_pk_bf16_f32 v188, v52, v53
	v_cvt_pk_bf16_f32 v189, v50, v51
	global_store_dwordx4 v[192:193], v[182:185], off
	global_store_dwordx4 v[192:193], v[186:189], off offset:256
	s_nop 0
	v_mov_b32_e32 v182, v248
	v_cvt_f32_i32_e32 v185, v47
	v_cvt_f32_i32_e32 v184, v46
	v_cvt_f32_i32_e32 v47, v49
	v_cvt_f32_i32_e32 v46, v48
	v_cvt_f32_i32_e32 v187, v43
	v_cvt_f32_i32_e32 v186, v42
	v_cvt_f32_i32_e32 v43, v45
	v_cvt_f32_i32_e32 v42, v44
	v_cvt_f32_i32_e32 v189, v39
	v_cvt_f32_i32_e32 v188, v38
	v_cvt_f32_i32_e32 v39, v41
	v_cvt_f32_i32_e32 v38, v40
	v_cvt_f32_i32_e32 v191, v35
	v_cvt_f32_i32_e32 v190, v34
	v_cvt_f32_i32_e32 v35, v37
	v_cvt_f32_i32_e32 v34, v36
	v_mad_i64_i32 v[36:37], s[34:35], v1, s64, v[150:151]
	v_lshl_add_u64 v[192:193], v[36:37], 0, v[170:171]
	v_add_u32_e32 v1, 0xa0, v148
	v_pk_mul_f32 v[36:37], v[154:155], v[182:183] op_sel_hi:[1,0]
	v_pk_mul_f32 v[40:41], v[156:157], v[182:183] op_sel_hi:[1,0]
	v_pk_mul_f32 v[44:45], v[158:159], v[182:183] op_sel_hi:[1,0]
	v_pk_mul_f32 v[196:197], v[160:161], v[182:183] op_sel_hi:[1,0]
	v_pk_mul_f32 v[198:199], v[162:163], v[182:183] op_sel_hi:[1,0]
	v_pk_mul_f32 v[200:201], v[164:165], v[182:183] op_sel_hi:[1,0]
	v_pk_mul_f32 v[202:203], v[166:167], v[182:183] op_sel_hi:[1,0]
	v_pk_mul_f32 v[182:183], v[168:169], v[182:183] op_sel_hi:[1,0]
	v_pk_mul_f32 v[46:47], v[40:41], v[46:47]
	v_pk_mul_f32 v[48:49], v[36:37], v[184:185]
	v_pk_mul_f32 v[42:43], v[196:197], v[42:43]
	v_pk_mul_f32 v[44:45], v[44:45], v[186:187]
	v_pk_mul_f32 v[38:39], v[200:201], v[38:39]
	v_pk_mul_f32 v[40:41], v[198:199], v[188:189]
	v_pk_mul_f32 v[34:35], v[182:183], v[34:35]
	v_pk_mul_f32 v[36:37], v[202:203], v[190:191]
	v_cvt_pk_bf16_f32 v182, v48, v49
	v_cvt_pk_bf16_f32 v183, v46, v47
	v_cvt_pk_bf16_f32 v184, v44, v45
	v_cvt_pk_bf16_f32 v185, v42, v43
	v_cvt_pk_bf16_f32 v186, v40, v41
	v_cvt_pk_bf16_f32 v187, v38, v39
	v_cvt_pk_bf16_f32 v188, v36, v37
	v_cvt_pk_bf16_f32 v189, v34, v35
	global_store_dwordx4 v[192:193], v[182:185], off
	global_store_dwordx4 v[192:193], v[186:189], off offset:256
	s_nop 0
	v_mov_b32_e32 v182, v249
	v_cvt_f32_i32_e32 v185, v31
	v_cvt_f32_i32_e32 v184, v30
	v_cvt_f32_i32_e32 v31, v33
	v_cvt_f32_i32_e32 v30, v32
	v_cvt_f32_i32_e32 v187, v27
	v_cvt_f32_i32_e32 v186, v26
	v_cvt_f32_i32_e32 v27, v29
	v_cvt_f32_i32_e32 v26, v28
	v_cvt_f32_i32_e32 v189, v15
	v_cvt_f32_i32_e32 v188, v14
	v_cvt_f32_i32_e32 v15, v17
	v_cvt_f32_i32_e32 v14, v16
	v_cvt_f32_i32_e32 v191, v11
	v_cvt_f32_i32_e32 v190, v10
	v_cvt_f32_i32_e32 v11, v13
	v_cvt_f32_i32_e32 v10, v12
	v_mad_i64_i32 v[12:13], s[34:35], v1, s64, v[150:151]
	v_lshl_add_u64 v[192:193], v[12:13], 0, v[170:171]
	v_add_u32_e32 v1, 0xb0, v148
	v_pk_mul_f32 v[12:13], v[154:155], v[182:183] op_sel_hi:[1,0]
	v_pk_mul_f32 v[16:17], v[156:157], v[182:183] op_sel_hi:[1,0]
	v_pk_mul_f32 v[28:29], v[158:159], v[182:183] op_sel_hi:[1,0]
	v_pk_mul_f32 v[196:197], v[160:161], v[182:183] op_sel_hi:[1,0]
	v_pk_mul_f32 v[198:199], v[162:163], v[182:183] op_sel_hi:[1,0]
	v_pk_mul_f32 v[200:201], v[164:165], v[182:183] op_sel_hi:[1,0]
	v_pk_mul_f32 v[202:203], v[166:167], v[182:183] op_sel_hi:[1,0]
	v_pk_mul_f32 v[182:183], v[168:169], v[182:183] op_sel_hi:[1,0]
	v_pk_mul_f32 v[30:31], v[16:17], v[30:31]
	v_pk_mul_f32 v[32:33], v[12:13], v[184:185]
	v_pk_mul_f32 v[26:27], v[196:197], v[26:27]
	v_pk_mul_f32 v[28:29], v[28:29], v[186:187]
	v_pk_mul_f32 v[14:15], v[200:201], v[14:15]
	v_pk_mul_f32 v[16:17], v[198:199], v[188:189]
	v_pk_mul_f32 v[10:11], v[182:183], v[10:11]
	v_pk_mul_f32 v[12:13], v[202:203], v[190:191]
	v_cvt_pk_bf16_f32 v182, v32, v33
	v_cvt_pk_bf16_f32 v183, v30, v31
	v_cvt_pk_bf16_f32 v184, v28, v29
	v_cvt_pk_bf16_f32 v185, v26, v27
	v_cvt_pk_bf16_f32 v186, v16, v17
	v_cvt_pk_bf16_f32 v187, v14, v15
	v_cvt_pk_bf16_f32 v188, v12, v13
	v_cvt_pk_bf16_f32 v189, v10, v11
	global_store_dwordx4 v[192:193], v[182:185], off
	global_store_dwordx4 v[192:193], v[186:189], off offset:256
	s_nop 0
	v_mov_b32_e32 v152, v250
	v_cvt_f32_i32_e32 v183, v23
	v_cvt_f32_i32_e32 v182, v22
	v_cvt_f32_i32_e32 v185, v25
	v_cvt_f32_i32_e32 v184, v24
	v_cvt_f32_i32_e32 v187, v19
	v_cvt_f32_i32_e32 v186, v18
	v_cvt_f32_i32_e32 v189, v21
	v_cvt_f32_i32_e32 v188, v20
	v_mad_i64_i32 v[18:19], s[34:35], v1, s64, v[150:151]
	v_lshl_add_u64 v[170:171], v[18:19], 0, v[170:171]
	v_pk_mul_f32 v[18:19], v[154:155], v[152:153] op_sel_hi:[1,0]
	v_pk_mul_f32 v[20:21], v[156:157], v[152:153] op_sel_hi:[1,0]
	v_pk_mul_f32 v[148:149], v[158:159], v[152:153] op_sel_hi:[1,0]
	v_pk_mul_f32 v[150:151], v[160:161], v[152:153] op_sel_hi:[1,0]
	v_pk_mul_f32 v[154:155], v[162:163], v[152:153] op_sel_hi:[1,0]
	v_pk_mul_f32 v[156:157], v[164:165], v[152:153] op_sel_hi:[1,0]
	v_pk_mul_f32 v[158:159], v[166:167], v[152:153] op_sel_hi:[1,0]
	v_pk_mul_f32 v[152:153], v[168:169], v[152:153] op_sel_hi:[1,0]
	v_pk_mul_f32 v[22:23], v[20:21], v[8:9]
	v_pk_mul_f32 v[24:25], v[18:19], v[6:7]
	v_pk_mul_f32 v[18:19], v[150:151], v[4:5]
	v_pk_mul_f32 v[20:21], v[148:149], v[2:3]
	v_pk_mul_f32 v[6:7], v[156:157], v[184:185]
	v_pk_mul_f32 v[8:9], v[154:155], v[182:183]
	v_pk_mul_f32 v[2:3], v[152:153], v[188:189]
	v_pk_mul_f32 v[4:5], v[158:159], v[186:187]
	v_cvt_pk_bf16_f32 v148, v24, v25
	v_cvt_pk_bf16_f32 v149, v22, v23
	v_cvt_pk_bf16_f32 v150, v20, v21
	v_cvt_pk_bf16_f32 v151, v18, v19
	v_cvt_pk_bf16_f32 v152, v8, v9
	v_cvt_pk_bf16_f32 v153, v6, v7
	v_cvt_pk_bf16_f32 v154, v4, v5
	v_cvt_pk_bf16_f32 v155, v2, v3
	global_store_dwordx4 v[170:171], v[148:151], off
	global_store_dwordx4 v[170:171], v[152:155], off offset:256
	s_cbranch_scc1 .LBB0_206
; __device__ __forceinline__ unsigned cvtpk(float lo, float hi) { f32x2 v = {lo, hi}; bf16x2_t b = __builtin_convertvector(v, bf16x2_t); return __builtin_bit_cast(unsigned, b); }
;     __device__ __forceinline__ void operator()(const f32x4 (&acc)[2][2][4][2], const Unit& u, int wr, int wc, int fr, int fq) const {
;     ...
;                         v[n] = (f32x4){(float)iv[0], (float)iv[1], (float)iv[2], (float)iv[3]} * (cmv[bj][n] * sa); cs[bj][n] += v[n]; }
;                     u32x4 w; w.x = cvtpk(v[0][0], v[0][1]); w.y = cvtpk(v[0][2], v[0][3]); w.z = cvtpk(v[1][0], v[1][1]); w.w = cvtpk(v[1][2], v[1][3]);
;                     *(u32x4*)(rowp + bj * HALF) = w; } }
;         if (u.pn == 2 || u.pn == 3) {
; #pragma unroll
;             for (int bj = 0; bj < 2; ++bj)
; #pragma unroll
;                 for (int n = 0; n < 2; ++n) {
; #pragma unroll
;                     for (int j = 0; j < 4; ++j) { float v = cs[bj][n][j]; v += __shfl_xor(v, 1); v += __shfl_xor(v, 2); v += __shfl_xor(v, 4); v += __shfl_xor(v, 8); cs[bj][n][j] = v; }
;                     if (fr == 0) { float* kp = kmean + (size_t)u.pm * 512 + (u.pn - 2) * BM + bj * HALF + wc * 32 + 8 * fq + 4 * n;
; #pragma unroll
;                         for (int j = 0; j < 4; ++j) atomicAdd(kp + j, cs[bj][n][j] * (1.f / 256.f)); } }
	v_pk_add_f32 v[128:129], v[128:129], 0 op_sel_hi:[1,0]
	v_pk_add_f32 v[126:127], v[126:127], 0 op_sel_hi:[1,0]
	v_pk_add_f32 v[110:111], v[128:129], v[110:111]
	v_pk_add_f32 v[112:113], v[126:127], v[112:113]
	v_pk_add_f32 v[94:95], v[110:111], v[94:95]
	v_pk_add_f32 v[96:97], v[112:113], v[96:97]
	v_pk_add_f32 v[78:79], v[94:95], v[78:79]
	v_pk_add_f32 v[80:81], v[96:97], v[80:81]
	v_pk_add_f32 v[62:63], v[78:79], v[62:63]
	v_pk_add_f32 v[64:65], v[80:81], v[64:65]
	v_pk_add_f32 v[46:47], v[62:63], v[46:47]
	v_xor_b32_e32 v1, 1, v180
	v_pk_add_f32 v[30:31], v[46:47], v[30:31]
	v_pk_add_f32 v[48:49], v[64:65], v[48:49]
	v_pk_add_f32 v[46:47], v[30:31], v[22:23]
	v_and_b32_e32 v22, 64, v180
	v_add_u32_e32 v30, 64, v22
	v_cmp_lt_i32_e32 vcc, v1, v30
	v_pk_add_f32 v[32:33], v[48:49], v[32:33]
	v_xor_b32_e32 v22, 2, v180
	v_cndmask_b32_e32 v1, v180, v1, vcc
	v_pk_add_f32 v[24:25], v[32:33], v[24:25]
	v_lshlrev_b32_e32 v1, 2, v1
	ds_bpermute_b32 v23, v1, v24
	v_cmp_lt_i32_e32 vcc, v22, v30
	v_xor_b32_e32 v31, 4, v180
	ds_bpermute_b32 v48, v1, v25
	v_cndmask_b32_e32 v22, v180, v22, vcc
	v_lshlrev_b32_e32 v22, 2, v22
	s_waitcnt lgkmcnt(1)
	v_add_f32_e32 v24, v24, v23
	ds_bpermute_b32 v32, v22, v24
	v_cmp_lt_i32_e32 vcc, v31, v30
	s_waitcnt lgkmcnt(1)
	v_add_f32_e32 v25, v25, v48
	ds_bpermute_b32 v48, v22, v25
	v_cndmask_b32_e32 v23, v180, v31, vcc
	v_lshlrev_b32_e32 v23, 2, v23
	s_waitcnt lgkmcnt(1)
	v_add_f32_e32 v32, v24, v32
	ds_bpermute_b32 v33, v23, v32
	v_xor_b32_e32 v31, 8, v180
	v_cmp_lt_i32_e32 vcc, v31, v30
	s_waitcnt lgkmcnt(1)
	v_add_f32_e32 v25, v25, v48
	ds_bpermute_b32 v48, v23, v25
	s_waitcnt lgkmcnt(1)
	v_add_f32_e32 v30, v32, v33
	ds_bpermute_b32 v32, v1, v46
	ds_bpermute_b32 v33, v1, v47
	v_cndmask_b32_e32 v24, v180, v31, vcc
	v_lshlrev_b32_e32 v24, 2, v24
	ds_bpermute_b32 v31, v24, v30
	s_waitcnt lgkmcnt(2)
	v_add_f32_e32 v32, v46, v32
	s_waitcnt lgkmcnt(1)
	v_add_f32_e32 v33, v47, v33
	ds_bpermute_b32 v46, v22, v32
	ds_bpermute_b32 v47, v22, v33
	s_ashr_i32 s31, s30, 31
	s_lshl_b64 s[30:31], s[30:31], 11
	s_waitcnt lgkmcnt(1)
	v_add_f32_e32 v46, v32, v46
	s_waitcnt lgkmcnt(0)
	v_add_f32_e32 v62, v33, v47
	ds_bpermute_b32 v49, v23, v46
	ds_bpermute_b32 v63, v23, v62
	v_add_f32_e32 v32, v25, v48
	ds_bpermute_b32 v33, v24, v32
	v_lshlrev_b32_e32 v25, 2, v130
	s_waitcnt lgkmcnt(2)
	v_add_f32_e32 v46, v46, v49
	s_waitcnt lgkmcnt(1)
	v_add_f32_e32 v48, v62, v63
	ds_bpermute_b32 v47, v24, v46
	ds_bpermute_b32 v49, v24, v48
	s_and_saveexec_b64 s[34:35], s[6:7]
	s_cbranch_execz .LBB0_199
	s_add_u32 s23, s52, s30
	s_addc_u32 s25, s53, s31
	s_lshl_b64 s[36:37], s[0:1], 2
	s_add_u32 s23, s23, s36
	s_addc_u32 s25, s25, s37
	s_lshl_b32 s36, s54, 2
	v_add_f32_e32 v30, v30, v31
	s_add_u32 s36, s23, s36
	s_waitcnt lgkmcnt(2)
	v_add_f32_e32 v31, v32, v33
	s_addc_u32 s37, s25, 0
	v_mul_f32_e32 v30, 0x3b800000, v30
	s_waitcnt lgkmcnt(1)
	v_add_f32_e32 v32, v46, v47
	global_atomic_add_f32 v25, v30, s[36:37] offset:-2048
	v_mul_f32_e32 v30, 0x3b800000, v31
	s_waitcnt lgkmcnt(0)
	v_add_f32_e32 v48, v48, v49
	global_atomic_add_f32 v25, v30, s[36:37] offset:-2044
	v_mul_f32_e32 v30, 0x3b800000, v32
	global_atomic_add_f32 v25, v30, s[36:37] offset:-2040
	v_mul_f32_e32 v30, 0x3b800000, v48
	global_atomic_add_f32 v25, v30, s[36:37] offset:-2036

;     __device__ __forceinline__ void operator()(const f32x4 (&acc)[2][2][4][2], const Unit& u, int wr, int wc, int fr, int fq) const {
;         const int row0 = u.pm * BM + wr * 64 + fr, col0 = u.pn * HALF + wc * 32 + 8 * fq;
;         const float* cm = colmax + (size_t)u.e * 2 * ldc + u.pn * BM + wc * 32 + 8 * fq;
;         const f32x4 cg0 = *(const f32x4*)(cm), cg1 = *(const f32x4*)(cm + 4), cu0 = *(const f32x4*)(cm + HALF), cu1 = *(const f32x4*)(cm + HALF + 4);
;         const float cg[8] = {cg0[0], cg0[1], cg0[2], cg0[3], cg1[0], cg1[1], cg1[2], cg1[3]}, cu[8] = {cu0[0], cu0[1], cu0[2], cu0[3], cu1[0], cu1[1], cu1[2], cu1[3]};
;         int cume = 0, cnte = 0x7fffffff; if (rowidx) { cume = tab[8 + u.e]; cnte = tab[u.e]; }
; #pragma unroll
;         for (int ai = 0; ai < 2; ++ai)
; #pragma unroll
;             for (int m = 0; m < 4; ++m) { const int r = row0 + ai * HALF + m * 16; unsigned char* rowp = O + (size_t)r * ldc + col0;
;                 float sa; if (rowidx) { const int rl = r - cume * BM; sa = (rl < cnte) ? rowmax[u.e * ECAP + rl] : 0.f; } else sa = rowmax[r];
;                 sa *= (1.f / (127.f * 127.f));
;                 float o[8];
; #pragma unroll
;                 for (int n = 0; n < 2; ++n)
; #pragma unroll
;                     for (int j = 0; j < 4; ++j) { const float g = (float)__builtin_bit_cast(i32x4, acc[ai][0][m][n])[j] * (sa * cg[n * 4 + j]), up = (float)__builtin_bit_cast(i32x4, acc[ai][1][m][n])[j] * (sa * cu[n * 4 + j]);
;                         o[n * 4 + j] = g * __builtin_amdgcn_rcpf(1.f + __builtin_amdgcn_exp2f(-1.4426950408889634f * g)) * up; }
;                 u32x2 w; w.x = pack_fp8x4(o[0], o[1], o[2], o[3]); w.y = pack_fp8x4(o[4], o[5], o[6], o[7]);
;                 *(u32x2*)rowp = w; }
.LBB0_1157:
	s_lshl_b32 s26, s55, 8
	v_lshl_add_u32 v160, s24, 8, v164
	s_ashr_i32 s27, s26, 31
	v_ashrrev_i32_e32 v161, 31, v160
	v_lshl_add_u64 v[66:67], s[26:27], 2, v[146:147]
	v_lshl_add_u64 v[162:163], v[160:161], 2, s[10:11]
	global_load_dword v1, v[162:163], off
	global_load_dword v244, v[162:163], off offset:64
	global_load_dword v245, v[162:163], off offset:128
	global_load_dword v246, v[162:163], off offset:192
	global_load_dword v247, v[162:163], off offset:512
	global_load_dword v248, v[162:163], off offset:576
	global_load_dword v249, v[162:163], off offset:640
	global_load_dword v250, v[162:163], off offset:704
	global_load_dwordx4 v[172:175], v[66:67], off offset:512
	global_load_dwordx4 v[70:73], v[66:67], off
	global_load_dwordx4 v[176:179], v[66:67], off offset:528
	s_nop 0
	global_load_dwordx4 v[66:69], v[66:67], off offset:16
	v_cvt_f32_i32_e32 v181, v134
	v_cvt_f32_i32_e32 v180, v130
	v_cvt_f32_i32_e32 v135, v135
	v_cvt_f32_i32_e32 v134, v131
	v_cvt_f32_i32_e32 v131, v136
	v_cvt_f32_i32_e32 v130, v132
	v_cvt_f32_i32_e32 v136, v133
	v_cvt_f32_i32_e32 v133, v126
	v_cvt_f32_i32_e32 v132, v122
	v_cvt_f32_i32_e32 v137, v137
	v_cvt_f32_i32_e32 v183, v127
	v_cvt_f32_i32_e32 v182, v123
	v_cvt_f32_i32_e32 v184, v124
	v_cvt_f32_i32_e32 v186, v125
	v_cvt_f32_i32_e32 v185, v128
	v_cvt_f32_i32_e32 v187, v129
	v_lshl_or_b32 v156, s55, 7, v166
	v_mov_b64_e32 v[158:159], s[58:59]
	v_ashrrev_i32_e32 v157, 31, v156
	v_cvt_f32_i32_e32 v121, v121
	v_cvt_f32_i32_e32 v113, v113
	v_cvt_f32_i32_e32 v119, v119
	v_cvt_f32_i32_e32 v111, v111
	v_cvt_f32_i32_e32 v103, v103
	v_cvt_f32_i32_e32 v95, v95
	v_cvt_f32_i32_e32 v105, v105
	v_cvt_f32_i32_e32 v97, v97
	v_cvt_f32_i32_e32 v87, v87
	v_cvt_f32_i32_e32 v79, v79
	v_cvt_f32_i32_e32 v89, v89
	v_cvt_f32_i32_e32 v81, v81
	v_cvt_f32_i32_e32 v63, v63
	v_cvt_f32_i32_e32 v65, v65
	v_cvt_f32_i32_e32 v55, v55
	v_cvt_f32_i32_e32 v57, v57
	v_cvt_f32_i32_e32 v47, v47
	v_cvt_f32_i32_e32 v39, v39
	v_cvt_f32_i32_e32 v41, v41
	v_cvt_f32_i32_e32 v49, v49
	v_cvt_f32_i32_e32 v31, v31
	v_cvt_f32_i32_e32 v23, v23
	v_cvt_f32_i32_e32 v25, v25
	v_cvt_f32_i32_e32 v33, v33
	v_cvt_f32_i32_e32 v7, v7
	v_cvt_f32_i32_e32 v9, v9
	v_cvt_f32_i32_e32 v3, v3
	v_cvt_f32_i32_e32 v5, v5
	s_andn2_b64 vcc, exec, s[6:7]
	s_mov_b64 s[6:7], -1
	s_waitcnt vmcnt(0)
	v_mul_f32_e32 v188, 0x38820610, v1
	v_mov_b32_e32 v122, v172
	v_mov_b32_e32 v123, v70
	v_mov_b32_e32 v70, v173
	v_mov_b32_e32 v126, v176
	v_mov_b32_e32 v127, v66
	v_mov_b32_e32 v124, v174
	v_mov_b32_e32 v125, v72
	v_mov_b32_e32 v72, v175
	v_pk_mul_f32 v[174:175], v[70:71], v[188:189] op_sel_hi:[1,0]
	v_pk_mul_f32 v[190:191], v[126:127], v[188:189] op_sel_hi:[1,0]
	v_mov_b32_e32 v66, v177
	v_pk_mul_f32 v[172:173], v[122:123], v[188:189] op_sel_hi:[1,0]
	v_pk_mul_f32 v[176:177], v[124:125], v[188:189] op_sel_hi:[1,0]
	v_pk_mul_f32 v[134:135], v[174:175], v[134:135]
	v_pk_mul_f32 v[132:133], v[190:191], v[132:133]
	v_mov_b32_e32 v128, v178
	v_mov_b32_e32 v129, v68
	v_mov_b32_e32 v68, v179
	v_pk_mul_f32 v[178:179], v[72:73], v[188:189] op_sel_hi:[1,0]
	v_pk_mul_f32 v[192:193], v[66:67], v[188:189] op_sel_hi:[1,0]
	v_pk_mul_f32 v[172:173], v[172:173], v[180:181]
	v_pk_mul_f32 v[130:131], v[176:177], v[130:131]
	v_mul_f32_e32 v161, 0xbfb8aa3b, v135
	v_mul_f32_e32 v181, 0xbfb8aa3b, v133
	v_pk_mul_f32 v[136:137], v[178:179], v[136:137]
	v_pk_mul_f32 v[174:175], v[192:193], v[182:183]
	v_mul_f32_e32 v1, 0xbfb8aa3b, v173
	v_mul_f32_e32 v171, 0xbfb8aa3b, v131
	v_exp_f32_e32 v161, v161
	v_exp_f32_e32 v181, v181
	v_mul_f32_e32 v180, 0xbfb8aa3b, v137
	v_mul_f32_e32 v182, 0xbfb8aa3b, v175
	v_exp_f32_e32 v1, v1
	v_exp_f32_e32 v171, v171
	v_exp_f32_e32 v180, v180
	v_exp_f32_e32 v182, v182
	v_pk_mul_f32 v[196:197], v[128:129], v[188:189] op_sel_hi:[1,0]
	v_pk_mul_f32 v[188:189], v[68:69], v[188:189] op_sel_hi:[1,0]
	v_pk_mul_f32 v[176:177], v[196:197], v[184:185]
	v_pk_mul_f32 v[178:179], v[188:189], v[186:187]
	v_add_f32_e32 v161, 1.0, v161
	v_add_f32_e32 v181, 1.0, v181
	v_mul_f32_e32 v183, 0xbfb8aa3b, v177
	v_mul_f32_e32 v184, 0xbfb8aa3b, v179
	v_add_f32_e32 v1, 1.0, v1
	v_add_f32_e32 v171, 1.0, v171
	v_rcp_f32_e32 v161, v161
	v_rcp_f32_e32 v181, v181
	v_exp_f32_e32 v183, v183
	v_exp_f32_e32 v184, v184
	v_add_f32_e32 v180, 1.0, v180
	v_add_f32_e32 v182, 1.0, v182
	v_rcp_f32_e32 v1, v1
	v_rcp_f32_e32 v171, v171
	v_rcp_f32_e32 v180, v180
	v_rcp_f32_e32 v182, v182
	v_mul_f32_e32 v135, v135, v161
	v_mul_f32_e32 v133, v133, v181
	v_mul_f32_e32 v1, v173, v1
	v_mul_f32_e32 v131, v131, v171
	v_mul_f32_e32 v134, v134, v135
	v_mul_f32_e32 v132, v132, v133
	v_add_f32_e32 v133, 1.0, v183
	v_add_f32_e32 v135, 1.0, v184
	v_mul_f32_e32 v137, v137, v180
	v_mul_f32_e32 v161, v175, v182
	v_mul_f32_e32 v1, v172, v1
	v_mul_f32_e32 v130, v130, v131
	v_rcp_f32_e32 v133, v133
	v_rcp_f32_e32 v135, v135
	v_mul_f32_e32 v131, v136, v137
	v_mul_f32_e32 v136, v174, v161
	v_med3_f32 v1, v1, s54, v170
	v_med3_f32 v134, v134, s54, v170
	v_med3_f32 v137, v130, s54, v170
	v_mov_b32_e32 v130, 0
	v_med3_f32 v161, v131, s54, v170
	v_cvt_pk_fp8_f32 v130, v1, v134
	v_med3_f32 v1, v132, s54, v170
	v_med3_f32 v132, v136, s54, v170
	v_mov_b32_e32 v131, 0
	v_cvt_pk_fp8_f32 v131, v1, v132
	v_mul_f32_e32 v133, v177, v133
	v_mul_f32_e32 v135, v179, v135
	v_mul_f32_e32 v133, v176, v133
	v_mul_f32_e32 v135, v178, v135
	v_med3_f32 v1, v133, s54, v170
	v_med3_f32 v132, v135, s54, v170
	v_cvt_pk_fp8_f32 v130, v137, v161 op_sel:[0,0,1]
	v_cvt_pk_fp8_f32 v131, v1, v132 op_sel:[0,0,1]
	v_mad_i64_i32 v[132:133], s[26:27], v160, s53, v[158:159]
	v_lshl_add_u64 v[132:133], v[132:133], 0, v[156:157]
	global_store_dwordx2 v[132:133], v[130:131], off
;     __device__ __forceinline__ void operator()(const f32x4 (&acc)[2][2][4][2], const Unit& u, int wr, int wc, int fr, int fq) const {
;     ...
;             for (int m = 0; m < 4; ++m) { const int r = row0 + ai * HALF + m * 16; unsigned char* rowp = O + (size_t)r * ldc + col0;
;                 float sa; if (rowidx) { const int rl = r - cume * BM; sa = (rl < cnte) ? rowmax[u.e * ECAP + rl] : 0.f; } else sa = rowmax[r];
;                 sa *= (1.f / (127.f * 127.f));
;                 float o[8];
; #pragma unroll
;                 for (int n = 0; n < 2; ++n)
; #pragma unroll
;                     for (int j = 0; j < 4; ++j) { const float g = (float)__builtin_bit_cast(i32x4, acc[ai][0][m][n])[j] * (sa * cg[n * 4 + j]), up = (float)__builtin_bit_cast(i32x4, acc[ai][1][m][n])[j] * (sa * cu[n * 4 + j]);
;                         o[n * 4 + j] = g * __builtin_amdgcn_rcpf(1.f + __builtin_amdgcn_exp2f(-1.4426950408889634f * g)) * up; }
;                 u32x2 w; w.x = pack_fp8x4(o[0], o[1], o[2], o[3]); w.y = pack_fp8x4(o[4], o[5], o[6], o[7]);
;                 *(u32x2*)rowp = w; }
	v_or_b32_e32 v130, 16, v160
	v_ashrrev_i32_e32 v131, 31, v130
	v_lshl_add_u64 v[132:133], v[130:131], 2, s[10:11]
	v_mov_b32_e32 v1, v244
	v_cvt_f32_i32_e32 v133, v118
	v_cvt_f32_i32_e32 v132, v114
	v_cvt_f32_i32_e32 v118, v115
	v_cvt_f32_i32_e32 v115, v120
	v_cvt_f32_i32_e32 v114, v116
	v_cvt_f32_i32_e32 v120, v117
	v_cvt_f32_i32_e32 v117, v110
	v_cvt_f32_i32_e32 v116, v106
	v_cvt_f32_i32_e32 v110, v107
	v_cvt_f32_i32_e32 v107, v112
	v_cvt_f32_i32_e32 v112, v109
	v_cvt_f32_i32_e32 v106, v108
	v_mul_f32_e32 v108, 0x38820610, v1
	v_pk_mul_f32 v[172:173], v[124:125], v[108:109] op_sel_hi:[1,0]
	v_pk_mul_f32 v[174:175], v[72:73], v[108:109] op_sel_hi:[1,0]
	v_pk_mul_f32 v[176:177], v[126:127], v[108:109] op_sel_hi:[1,0]
	v_pk_mul_f32 v[134:135], v[122:123], v[108:109] op_sel_hi:[1,0]
	v_pk_mul_f32 v[136:137], v[70:71], v[108:109] op_sel_hi:[1,0]
	v_pk_mul_f32 v[178:179], v[66:67], v[108:109] op_sel_hi:[1,0]
	v_pk_mul_f32 v[180:181], v[128:129], v[108:109] op_sel_hi:[1,0]
	v_pk_mul_f32 v[108:109], v[68:69], v[108:109] op_sel_hi:[1,0]
	v_pk_mul_f32 v[114:115], v[172:173], v[114:115]
	v_pk_mul_f32 v[120:121], v[174:175], v[120:121]
	v_pk_mul_f32 v[116:117], v[176:177], v[116:117]
	v_pk_mul_f32 v[132:133], v[134:135], v[132:133]
	v_pk_mul_f32 v[108:109], v[108:109], v[112:113]
	v_mul_f32_e32 v113, 0xbfb8aa3b, v115
	v_mul_f32_e32 v131, 0xbfb8aa3b, v121
	v_mul_f32_e32 v134, 0xbfb8aa3b, v117
	v_exp_f32_e32 v113, v113
	v_exp_f32_e32 v131, v131
	v_exp_f32_e32 v134, v134
	v_pk_mul_f32 v[118:119], v[136:137], v[118:119]
	v_pk_mul_f32 v[110:111], v[178:179], v[110:111]
	v_pk_mul_f32 v[106:107], v[180:181], v[106:107]
	v_mul_f32_e32 v1, 0xbfb8aa3b, v133
	v_mul_f32_e32 v112, 0xbfb8aa3b, v119
	v_mul_f32_e32 v135, 0xbfb8aa3b, v111
	v_mul_f32_e32 v136, 0xbfb8aa3b, v107
	v_add_f32_e32 v113, 1.0, v113
	v_add_f32_e32 v131, 1.0, v131
	v_add_f32_e32 v134, 1.0, v134
	v_mul_f32_e32 v137, 0xbfb8aa3b, v109
	v_exp_f32_e32 v1, v1
	v_exp_f32_e32 v112, v112
	v_exp_f32_e32 v135, v135
	v_exp_f32_e32 v136, v136
	v_rcp_f32_e32 v113, v113
	v_rcp_f32_e32 v131, v131
	v_rcp_f32_e32 v134, v134
	v_exp_f32_e32 v137, v137
	v_add_f32_e32 v1, 1.0, v1
	v_add_f32_e32 v112, 1.0, v112
	v_add_f32_e32 v135, 1.0, v135
	v_add_f32_e32 v136, 1.0, v136
	v_mul_f32_e32 v113, v115, v113
	v_mul_f32_e32 v115, v121, v131
	v_mul_f32_e32 v117, v117, v134
	v_rcp_f32_e32 v1, v1
	v_rcp_f32_e32 v112, v112
	v_rcp_f32_e32 v135, v135
	v_rcp_f32_e32 v136, v136
	v_mul_f32_e32 v113, v114, v113
	v_mul_f32_e32 v114, v120, v115
	v_mul_f32_e32 v115, v116, v117
	v_add_f32_e32 v116, 1.0, v137
	v_rcp_f32_e32 v116, v116
	v_mul_f32_e32 v1, v133, v1
	v_mul_f32_e32 v112, v119, v112
	v_mul_f32_e32 v111, v111, v135
	v_mul_f32_e32 v107, v107, v136
	v_mul_f32_e32 v1, v132, v1
	v_mul_f32_e32 v112, v118, v112
	v_mul_f32_e32 v110, v110, v111
	v_mul_f32_e32 v111, v106, v107
	v_mul_f32_e32 v106, v109, v116
	v_mul_f32_e32 v108, v108, v106
	v_med3_f32 v1, v1, s54, v170
	v_med3_f32 v107, v112, s54, v170
	v_mov_b32_e32 v106, 0
	v_cvt_pk_fp8_f32 v106, v1, v107
	v_med3_f32 v1, v115, s54, v170
	v_med3_f32 v110, v110, s54, v170
	v_mov_b32_e32 v107, 0
	v_cvt_pk_fp8_f32 v107, v1, v110
	v_med3_f32 v109, v113, s54, v170
	v_med3_f32 v112, v114, s54, v170
	v_med3_f32 v1, v111, s54, v170
	v_med3_f32 v108, v108, s54, v170
	v_cvt_pk_fp8_f32 v106, v109, v112 op_sel:[0,0,1]
	v_cvt_pk_fp8_f32 v107, v1, v108 op_sel:[0,0,1]
	v_mad_i64_i32 v[108:109], s[26:27], v130, s53, v[158:159]
	v_lshl_add_u64 v[108:109], v[108:109], 0, v[156:157]
	global_store_dwordx2 v[108:109], v[106:107], off
	v_or_b32_e32 v106, 32, v160
	v_ashrrev_i32_e32 v107, 31, v106
	v_lshl_add_u64 v[108:109], v[106:107], 2, s[10:11]
	v_mov_b32_e32 v1, v245
	v_cvt_f32_i32_e32 v109, v102
	v_cvt_f32_i32_e32 v108, v98
	v_cvt_f32_i32_e32 v102, v99
	v_cvt_f32_i32_e32 v99, v104
	v_cvt_f32_i32_e32 v98, v100
	v_cvt_f32_i32_e32 v104, v101
	v_cvt_f32_i32_e32 v101, v94
	v_cvt_f32_i32_e32 v100, v90
	v_cvt_f32_i32_e32 v94, v91
	v_cvt_f32_i32_e32 v91, v96
	v_cvt_f32_i32_e32 v90, v92
	v_cvt_f32_i32_e32 v96, v93
	v_mul_f32_e32 v92, 0x38820610, v1
	v_pk_mul_f32 v[110:111], v[122:123], v[92:93] op_sel_hi:[1,0]
	v_pk_mul_f32 v[112:113], v[70:71], v[92:93] op_sel_hi:[1,0]
	v_pk_mul_f32 v[120:121], v[66:67], v[92:93] op_sel_hi:[1,0]
	v_pk_mul_f32 v[130:131], v[128:129], v[92:93] op_sel_hi:[1,0]
	v_pk_mul_f32 v[114:115], v[124:125], v[92:93] op_sel_hi:[1,0]
	v_pk_mul_f32 v[116:117], v[72:73], v[92:93] op_sel_hi:[1,0]
	v_pk_mul_f32 v[118:119], v[126:127], v[92:93] op_sel_hi:[1,0]
	v_pk_mul_f32 v[92:93], v[68:69], v[92:93] op_sel_hi:[1,0]
	v_pk_mul_f32 v[108:109], v[110:111], v[108:109]
	v_pk_mul_f32 v[102:103], v[112:113], v[102:103]
	v_pk_mul_f32 v[94:95], v[120:121], v[94:95]
	v_pk_mul_f32 v[90:91], v[130:131], v[90:91]
	v_pk_mul_f32 v[98:99], v[114:115], v[98:99]
	v_pk_mul_f32 v[104:105], v[116:117], v[104:105]
	v_pk_mul_f32 v[100:101], v[118:119], v[100:101]
	v_pk_mul_f32 v[92:93], v[92:93], v[96:97]
	v_mul_f32_e32 v1, 0xbfb8aa3b, v109
	v_mul_f32_e32 v96, 0xbfb8aa3b, v103
	v_mul_f32_e32 v111, 0xbfb8aa3b, v95
	v_mul_f32_e32 v112, 0xbfb8aa3b, v91
	v_mul_f32_e32 v97, 0xbfb8aa3b, v99
	v_mul_f32_e32 v107, 0xbfb8aa3b, v105
	v_mul_f32_e32 v110, 0xbfb8aa3b, v101
	v_mul_f32_e32 v113, 0xbfb8aa3b, v93
	v_exp_f32_e32 v1, v1
	v_exp_f32_e32 v96, v96
	v_exp_f32_e32 v111, v111
	v_exp_f32_e32 v112, v112
	v_exp_f32_e32 v97, v97
	v_exp_f32_e32 v107, v107
	v_exp_f32_e32 v110, v110
	v_exp_f32_e32 v113, v113
	v_add_f32_e32 v1, 1.0, v1
	v_add_f32_e32 v96, 1.0, v96
	v_add_f32_e32 v111, 1.0, v111
	v_add_f32_e32 v112, 1.0, v112
	v_add_f32_e32 v97, 1.0, v97
	v_add_f32_e32 v107, 1.0, v107
	v_add_f32_e32 v110, 1.0, v110
;     __device__ __forceinline__ void operator()(const f32x4 (&acc)[2][2][4][2], const Unit& u, int wr, int wc, int fr, int fq) const {
;     ...
;             for (int m = 0; m < 4; ++m) { const int r = row0 + ai * HALF + m * 16; unsigned char* rowp = O + (size_t)r * ldc + col0;
;                 float sa; if (rowidx) { const int rl = r - cume * BM; sa = (rl < cnte) ? rowmax[u.e * ECAP + rl] : 0.f; } else sa = rowmax[r];
;                 sa *= (1.f / (127.f * 127.f));
;                 float o[8];
; #pragma unroll
;                 for (int n = 0; n < 2; ++n)
; #pragma unroll
;                     for (int j = 0; j < 4; ++j) { const float g = (float)__builtin_bit_cast(i32x4, acc[ai][0][m][n])[j] * (sa * cg[n * 4 + j]), up = (float)__builtin_bit_cast(i32x4, acc[ai][1][m][n])[j] * (sa * cu[n * 4 + j]);
;                         o[n * 4 + j] = g * __builtin_amdgcn_rcpf(1.f + __builtin_amdgcn_exp2f(-1.4426950408889634f * g)) * up; }
;                 u32x2 w; w.x = pack_fp8x4(o[0], o[1], o[2], o[3]); w.y = pack_fp8x4(o[4], o[5], o[6], o[7]);
;                 *(u32x2*)rowp = w; }
	v_add_f32_e32 v113, 1.0, v113
	v_rcp_f32_e32 v1, v1
	v_rcp_f32_e32 v96, v96
	v_rcp_f32_e32 v111, v111
	v_rcp_f32_e32 v112, v112
	v_rcp_f32_e32 v97, v97
	v_rcp_f32_e32 v107, v107
	v_rcp_f32_e32 v110, v110
	v_rcp_f32_e32 v113, v113
	v_mul_f32_e32 v1, v109, v1
	v_mul_f32_e32 v96, v103, v96
	v_mul_f32_e32 v95, v95, v111
	v_mul_f32_e32 v91, v91, v112
	v_mul_f32_e32 v97, v99, v97
	v_mul_f32_e32 v99, v105, v107
	v_mul_f32_e32 v101, v101, v110
	v_mul_f32_e32 v1, v108, v1
	v_mul_f32_e32 v96, v102, v96
	v_mul_f32_e32 v94, v94, v95
	v_mul_f32_e32 v95, v90, v91
	v_mul_f32_e32 v90, v93, v113
	v_mul_f32_e32 v97, v98, v97
	v_mul_f32_e32 v98, v104, v99
	v_mul_f32_e32 v99, v100, v101
	v_mul_f32_e32 v92, v92, v90
	v_med3_f32 v1, v1, s54, v170
	v_med3_f32 v91, v96, s54, v170
	v_mov_b32_e32 v90, 0
	v_cvt_pk_fp8_f32 v90, v1, v91
	v_med3_f32 v1, v99, s54, v170
	v_med3_f32 v94, v94, s54, v170
	v_mov_b32_e32 v91, 0
	v_cvt_pk_fp8_f32 v91, v1, v94
	v_med3_f32 v93, v97, s54, v170
	v_med3_f32 v96, v98, s54, v170
	v_med3_f32 v1, v95, s54, v170
	v_med3_f32 v92, v92, s54, v170
	v_cvt_pk_fp8_f32 v90, v93, v96 op_sel:[0,0,1]
	v_cvt_pk_fp8_f32 v91, v1, v92 op_sel:[0,0,1]
	v_mad_i64_i32 v[92:93], s[26:27], v106, s53, v[158:159]
	v_lshl_add_u64 v[92:93], v[92:93], 0, v[156:157]
	global_store_dwordx2 v[92:93], v[90:91], off
	v_or_b32_e32 v90, 48, v160
	v_ashrrev_i32_e32 v91, 31, v90
	v_lshl_add_u64 v[92:93], v[90:91], 2, s[10:11]
	v_mov_b32_e32 v1, v246
	v_cvt_f32_i32_e32 v93, v86
	v_cvt_f32_i32_e32 v92, v82
	v_cvt_f32_i32_e32 v86, v83
	v_cvt_f32_i32_e32 v83, v88
	v_cvt_f32_i32_e32 v82, v84
	v_cvt_f32_i32_e32 v88, v85
	v_cvt_f32_i32_e32 v85, v78
	v_cvt_f32_i32_e32 v84, v74
	v_cvt_f32_i32_e32 v78, v75
	v_cvt_f32_i32_e32 v75, v80
	v_cvt_f32_i32_e32 v74, v76
	v_cvt_f32_i32_e32 v80, v77
	v_mul_f32_e32 v76, 0x38820610, v1
	v_pk_mul_f32 v[94:95], v[122:123], v[76:77] op_sel_hi:[1,0]
	v_pk_mul_f32 v[96:97], v[70:71], v[76:77] op_sel_hi:[1,0]
	v_pk_mul_f32 v[104:105], v[66:67], v[76:77] op_sel_hi:[1,0]
	v_pk_mul_f32 v[106:107], v[128:129], v[76:77] op_sel_hi:[1,0]
	v_pk_mul_f32 v[98:99], v[124:125], v[76:77] op_sel_hi:[1,0]
	v_pk_mul_f32 v[100:101], v[72:73], v[76:77] op_sel_hi:[1,0]
	v_pk_mul_f32 v[102:103], v[126:127], v[76:77] op_sel_hi:[1,0]
	v_pk_mul_f32 v[76:77], v[68:69], v[76:77] op_sel_hi:[1,0]
	v_pk_mul_f32 v[92:93], v[94:95], v[92:93]
	v_pk_mul_f32 v[86:87], v[96:97], v[86:87]
	v_pk_mul_f32 v[78:79], v[104:105], v[78:79]
	v_pk_mul_f32 v[74:75], v[106:107], v[74:75]
	v_pk_mul_f32 v[82:83], v[98:99], v[82:83]
	v_pk_mul_f32 v[88:89], v[100:101], v[88:89]
	v_pk_mul_f32 v[84:85], v[102:103], v[84:85]
	v_pk_mul_f32 v[76:77], v[76:77], v[80:81]
	v_mul_f32_e32 v1, 0xbfb8aa3b, v93
	v_mul_f32_e32 v80, 0xbfb8aa3b, v87
	v_mul_f32_e32 v95, 0xbfb8aa3b, v79
	v_mul_f32_e32 v96, 0xbfb8aa3b, v75
	v_mul_f32_e32 v81, 0xbfb8aa3b, v83
	v_mul_f32_e32 v91, 0xbfb8aa3b, v89
	v_mul_f32_e32 v94, 0xbfb8aa3b, v85
	v_mul_f32_e32 v97, 0xbfb8aa3b, v77
	v_exp_f32_e32 v1, v1
	v_exp_f32_e32 v80, v80
	v_exp_f32_e32 v95, v95
	v_exp_f32_e32 v96, v96
	v_exp_f32_e32 v81, v81
	v_exp_f32_e32 v91, v91
	v_exp_f32_e32 v94, v94
	v_exp_f32_e32 v97, v97
	v_add_f32_e32 v1, 1.0, v1
	v_add_f32_e32 v80, 1.0, v80
	v_add_f32_e32 v95, 1.0, v95
	v_add_f32_e32 v96, 1.0, v96
	v_add_f32_e32 v81, 1.0, v81
	v_add_f32_e32 v91, 1.0, v91
	v_add_f32_e32 v94, 1.0, v94
	v_add_f32_e32 v97, 1.0, v97
	v_rcp_f32_e32 v1, v1
	v_rcp_f32_e32 v80, v80
	v_rcp_f32_e32 v95, v95
	v_rcp_f32_e32 v96, v96
	v_rcp_f32_e32 v81, v81
	v_rcp_f32_e32 v91, v91
	v_rcp_f32_e32 v94, v94
	v_rcp_f32_e32 v97, v97
	v_mul_f32_e32 v1, v93, v1
	v_mul_f32_e32 v80, v87, v80
	v_mul_f32_e32 v79, v79, v95
	v_mul_f32_e32 v75, v75, v96
	v_mul_f32_e32 v81, v83, v81
	v_mul_f32_e32 v83, v89, v91
	v_mul_f32_e32 v85, v85, v94
	v_mul_f32_e32 v1, v92, v1
	v_mul_f32_e32 v80, v86, v80
	v_mul_f32_e32 v78, v78, v79
	v_mul_f32_e32 v79, v74, v75
	v_mul_f32_e32 v74, v77, v97
	v_mul_f32_e32 v81, v82, v81
	v_mul_f32_e32 v82, v88, v83
	v_mul_f32_e32 v83, v84, v85
	v_mul_f32_e32 v76, v76, v74
	v_med3_f32 v1, v1, s54, v170
	v_med3_f32 v75, v80, s54, v170
	v_mov_b32_e32 v74, 0
	v_cvt_pk_fp8_f32 v74, v1, v75
	v_med3_f32 v1, v83, s54, v170
	v_med3_f32 v78, v78, s54, v170
	v_mov_b32_e32 v75, 0
	v_cvt_pk_fp8_f32 v75, v1, v78
	v_med3_f32 v77, v81, s54, v170
	v_med3_f32 v80, v82, s54, v170
	v_med3_f32 v1, v79, s54, v170
	v_med3_f32 v76, v76, s54, v170
	v_cvt_pk_fp8_f32 v74, v77, v80 op_sel:[0,0,1]
	v_cvt_pk_fp8_f32 v75, v1, v76 op_sel:[0,0,1]
	v_mad_i64_i32 v[76:77], s[26:27], v90, s53, v[158:159]
	v_lshl_add_u64 v[76:77], v[76:77], 0, v[156:157]
	global_store_dwordx2 v[76:77], v[74:75], off
	v_mov_b32_e32 v1, v247
	v_cvt_f32_i32_e32 v75, v62
	v_cvt_f32_i32_e32 v74, v58
	v_cvt_f32_i32_e32 v62, v59
	v_cvt_f32_i32_e32 v59, v64
	v_cvt_f32_i32_e32 v58, v60
	v_cvt_f32_i32_e32 v64, v61
	v_cvt_f32_i32_e32 v61, v54
	v_cvt_f32_i32_e32 v60, v50
	v_cvt_f32_i32_e32 v54, v51
	v_cvt_f32_i32_e32 v51, v56
	v_cvt_f32_i32_e32 v50, v52
	v_cvt_f32_i32_e32 v56, v53
	v_add_u32_e32 v90, 0x80, v160
	v_mul_f32_e32 v52, 0x38820610, v1
	v_pk_mul_f32 v[76:77], v[122:123], v[52:53] op_sel_hi:[1,0]
	v_pk_mul_f32 v[78:79], v[70:71], v[52:53] op_sel_hi:[1,0]
	v_pk_mul_f32 v[80:81], v[124:125], v[52:53] op_sel_hi:[1,0]
	v_pk_mul_f32 v[82:83], v[72:73], v[52:53] op_sel_hi:[1,0]
	v_pk_mul_f32 v[84:85], v[126:127], v[52:53] op_sel_hi:[1,0]
	v_pk_mul_f32 v[86:87], v[66:67], v[52:53] op_sel_hi:[1,0]
	v_pk_mul_f32 v[88:89], v[128:129], v[52:53] op_sel_hi:[1,0]
	v_pk_mul_f32 v[52:53], v[68:69], v[52:53] op_sel_hi:[1,0]
	v_pk_mul_f32 v[74:75], v[76:77], v[74:75]
	v_pk_mul_f32 v[62:63], v[78:79], v[62:63]
	v_pk_mul_f32 v[58:59], v[80:81], v[58:59]
;     __device__ __forceinline__ void operator()(const f32x4 (&acc)[2][2][4][2], const Unit& u, int wr, int wc, int fr, int fq) const {
;     ...
;             for (int m = 0; m < 4; ++m) { const int r = row0 + ai * HALF + m * 16; unsigned char* rowp = O + (size_t)r * ldc + col0;
;                 float sa; if (rowidx) { const int rl = r - cume * BM; sa = (rl < cnte) ? rowmax[u.e * ECAP + rl] : 0.f; } else sa = rowmax[r];
;                 sa *= (1.f / (127.f * 127.f));
;                 float o[8];
; #pragma unroll
;                 for (int n = 0; n < 2; ++n)
; #pragma unroll
;                     for (int j = 0; j < 4; ++j) { const float g = (float)__builtin_bit_cast(i32x4, acc[ai][0][m][n])[j] * (sa * cg[n * 4 + j]), up = (float)__builtin_bit_cast(i32x4, acc[ai][1][m][n])[j] * (sa * cu[n * 4 + j]);
;                         o[n * 4 + j] = g * __builtin_amdgcn_rcpf(1.f + __builtin_amdgcn_exp2f(-1.4426950408889634f * g)) * up; }
;                 u32x2 w; w.x = pack_fp8x4(o[0], o[1], o[2], o[3]); w.y = pack_fp8x4(o[4], o[5], o[6], o[7]);
;                 *(u32x2*)rowp = w; }
	v_pk_mul_f32 v[64:65], v[82:83], v[64:65]
	v_pk_mul_f32 v[60:61], v[84:85], v[60:61]
	v_pk_mul_f32 v[54:55], v[86:87], v[54:55]
	v_pk_mul_f32 v[50:51], v[88:89], v[50:51]
	v_pk_mul_f32 v[52:53], v[52:53], v[56:57]
	v_mul_f32_e32 v1, 0xbfb8aa3b, v75
	v_mul_f32_e32 v56, 0xbfb8aa3b, v63
	v_mul_f32_e32 v57, 0xbfb8aa3b, v59
	v_mul_f32_e32 v76, 0xbfb8aa3b, v65
	v_mul_f32_e32 v77, 0xbfb8aa3b, v61
	v_mul_f32_e32 v78, 0xbfb8aa3b, v55
	v_mul_f32_e32 v79, 0xbfb8aa3b, v51
	v_exp_f32_e32 v1, v1
	v_exp_f32_e32 v56, v56
	v_exp_f32_e32 v57, v57
	v_exp_f32_e32 v76, v76
	v_exp_f32_e32 v77, v77
	v_exp_f32_e32 v78, v78
	v_exp_f32_e32 v79, v79
	v_mul_f32_e32 v80, 0xbfb8aa3b, v53
	v_add_f32_e32 v1, 1.0, v1
	v_add_f32_e32 v56, 1.0, v56
	v_exp_f32_e32 v80, v80
	v_add_f32_e32 v57, 1.0, v57
	v_add_f32_e32 v76, 1.0, v76
	v_add_f32_e32 v77, 1.0, v77
	v_add_f32_e32 v78, 1.0, v78
	v_add_f32_e32 v79, 1.0, v79
	v_rcp_f32_e32 v1, v1
	v_rcp_f32_e32 v56, v56
	v_rcp_f32_e32 v57, v57
	v_rcp_f32_e32 v76, v76
	v_rcp_f32_e32 v77, v77
	v_rcp_f32_e32 v78, v78
	v_rcp_f32_e32 v79, v79
	v_add_f32_e32 v80, 1.0, v80
	v_mul_f32_e32 v1, v75, v1
	v_mul_f32_e32 v56, v63, v56
	v_rcp_f32_e32 v80, v80
	v_mul_f32_e32 v57, v59, v57
	v_mul_f32_e32 v59, v65, v76
	v_mul_f32_e32 v61, v61, v77
	v_mul_f32_e32 v55, v55, v78
	v_mul_f32_e32 v51, v51, v79
	v_mul_f32_e32 v1, v74, v1
	v_mul_f32_e32 v56, v62, v56
	v_mul_f32_e32 v57, v58, v57
	v_mul_f32_e32 v58, v64, v59
	v_mul_f32_e32 v59, v60, v61
	v_mul_f32_e32 v54, v54, v55
	v_mul_f32_e32 v55, v50, v51
	v_med3_f32 v1, v1, s54, v170
	v_med3_f32 v51, v56, s54, v170
	v_mov_b32_e32 v50, 0
	v_cvt_pk_fp8_f32 v50, v1, v51
	v_med3_f32 v1, v59, s54, v170
	v_med3_f32 v54, v54, s54, v170
	v_mov_b32_e32 v51, 0
	v_cvt_pk_fp8_f32 v51, v1, v54
	v_mul_f32_e32 v53, v53, v80
	v_mul_f32_e32 v52, v52, v53
	v_med3_f32 v53, v57, s54, v170
	v_med3_f32 v56, v58, s54, v170
	v_med3_f32 v1, v55, s54, v170
	v_med3_f32 v52, v52, s54, v170
	v_cvt_pk_fp8_f32 v50, v53, v56 op_sel:[0,0,1]
	v_cvt_pk_fp8_f32 v51, v1, v52 op_sel:[0,0,1]
	v_mad_i64_i32 v[52:53], s[26:27], v90, s53, v[158:159]
	v_lshl_add_u64 v[52:53], v[52:53], 0, v[156:157]
	global_store_dwordx2 v[52:53], v[50:51], off
	v_mov_b32_e32 v1, v248
	v_cvt_f32_i32_e32 v51, v46
	v_cvt_f32_i32_e32 v50, v42
	v_cvt_f32_i32_e32 v46, v43
	v_cvt_f32_i32_e32 v43, v48
	v_cvt_f32_i32_e32 v42, v44
	v_cvt_f32_i32_e32 v48, v45
	v_cvt_f32_i32_e32 v45, v38
	v_cvt_f32_i32_e32 v44, v34
	v_cvt_f32_i32_e32 v38, v35
	v_cvt_f32_i32_e32 v35, v40
	v_cvt_f32_i32_e32 v40, v37
	v_cvt_f32_i32_e32 v34, v36
	v_mov_b32_e32 v36, 0
	v_mov_b32_e32 v37, 0
	v_add_u32_e32 v76, 0x90, v160
	v_mul_f32_e32 v52, 0x38820610, v1
	v_pk_mul_f32 v[54:55], v[122:123], v[52:53] op_sel_hi:[1,0]
	v_pk_mul_f32 v[56:57], v[70:71], v[52:53] op_sel_hi:[1,0]
	v_pk_mul_f32 v[58:59], v[124:125], v[52:53] op_sel_hi:[1,0]
	v_pk_mul_f32 v[60:61], v[72:73], v[52:53] op_sel_hi:[1,0]
	v_pk_mul_f32 v[62:63], v[126:127], v[52:53] op_sel_hi:[1,0]
	v_pk_mul_f32 v[64:65], v[66:67], v[52:53] op_sel_hi:[1,0]
	v_pk_mul_f32 v[74:75], v[128:129], v[52:53] op_sel_hi:[1,0]
	v_pk_mul_f32 v[52:53], v[68:69], v[52:53] op_sel_hi:[1,0]
	v_pk_mul_f32 v[50:51], v[54:55], v[50:51]
	v_pk_mul_f32 v[46:47], v[56:57], v[46:47]
	v_pk_mul_f32 v[44:45], v[62:63], v[44:45]
	v_pk_mul_f32 v[38:39], v[64:65], v[38:39]
	v_pk_mul_f32 v[40:41], v[52:53], v[40:41]
	v_mul_f32_e32 v1, 0xbfb8aa3b, v51
	v_mul_f32_e32 v52, 0xbfb8aa3b, v47
	v_mul_f32_e32 v55, 0xbfb8aa3b, v45
	v_mul_f32_e32 v56, 0xbfb8aa3b, v39
	v_exp_f32_e32 v1, v1
	v_exp_f32_e32 v52, v52
	v_exp_f32_e32 v55, v55
	v_exp_f32_e32 v56, v56
	v_pk_mul_f32 v[42:43], v[58:59], v[42:43]
	v_pk_mul_f32 v[48:49], v[60:61], v[48:49]
	v_pk_mul_f32 v[34:35], v[74:75], v[34:35]
	v_mul_f32_e32 v53, 0xbfb8aa3b, v43
	v_mul_f32_e32 v54, 0xbfb8aa3b, v49
	v_mul_f32_e32 v57, 0xbfb8aa3b, v35
	v_mul_f32_e32 v58, 0xbfb8aa3b, v41
	v_add_f32_e32 v1, 1.0, v1
	v_add_f32_e32 v52, 1.0, v52
	v_exp_f32_e32 v53, v53
	v_exp_f32_e32 v54, v54
	v_exp_f32_e32 v57, v57
	v_exp_f32_e32 v58, v58
	v_add_f32_e32 v55, 1.0, v55
	v_add_f32_e32 v56, 1.0, v56
	v_rcp_f32_e32 v1, v1
	v_rcp_f32_e32 v52, v52
	v_rcp_f32_e32 v55, v55
	v_rcp_f32_e32 v56, v56
	v_add_f32_e32 v53, 1.0, v53
	v_add_f32_e32 v54, 1.0, v54
	v_add_f32_e32 v57, 1.0, v57
	v_add_f32_e32 v58, 1.0, v58
	v_mul_f32_e32 v1, v51, v1
	v_mul_f32_e32 v47, v47, v52
	v_rcp_f32_e32 v53, v53
	v_rcp_f32_e32 v54, v54
	v_rcp_f32_e32 v57, v57
	v_rcp_f32_e32 v58, v58
	v_mul_f32_e32 v45, v45, v55
	v_mul_f32_e32 v39, v39, v56
	v_mul_f32_e32 v1, v50, v1
	v_mul_f32_e32 v46, v46, v47
	v_mul_f32_e32 v44, v44, v45
	v_mul_f32_e32 v38, v38, v39
	v_med3_f32 v1, v1, s54, v170
	v_med3_f32 v39, v46, s54, v170
	v_cvt_pk_fp8_f32 v36, v1, v39
	v_med3_f32 v1, v44, s54, v170
	v_med3_f32 v38, v38, s54, v170
	v_cvt_pk_fp8_f32 v37, v1, v38
	v_mul_f32_e32 v43, v43, v53
	v_mul_f32_e32 v49, v49, v54
	v_mul_f32_e32 v35, v35, v57
	v_mul_f32_e32 v41, v41, v58
	v_mul_f32_e32 v42, v42, v43
	v_mul_f32_e32 v43, v48, v49
	v_mul_f32_e32 v34, v34, v35
	v_mul_f32_e32 v35, v40, v41
	v_med3_f32 v40, v42, s54, v170
	v_med3_f32 v41, v43, s54, v170
	v_med3_f32 v1, v34, s54, v170
	v_med3_f32 v34, v35, s54, v170
	v_cvt_pk_fp8_f32 v36, v40, v41 op_sel:[0,0,1]
	v_cvt_pk_fp8_f32 v37, v1, v34 op_sel:[0,0,1]
	v_mad_i64_i32 v[34:35], s[26:27], v76, s53, v[158:159]
	v_lshl_add_u64 v[34:35], v[34:35], 0, v[156:157]
	global_store_dwordx2 v[34:35], v[36:37], off
	v_mov_b32_e32 v1, v249
	v_cvt_f32_i32_e32 v35, v30
	v_cvt_f32_i32_e32 v34, v26
	v_cvt_f32_i32_e32 v30, v27
	v_cvt_f32_i32_e32 v27, v32
	v_cvt_f32_i32_e32 v26, v28
	v_cvt_f32_i32_e32 v32, v29
	v_cvt_f32_i32_e32 v29, v22
	v_cvt_f32_i32_e32 v28, v18
;     __device__ __forceinline__ void operator()(const f32x4 (&acc)[2][2][4][2], const Unit& u, int wr, int wc, int fr, int fq) const {
;     ...
;             for (int m = 0; m < 4; ++m) { const int r = row0 + ai * HALF + m * 16; unsigned char* rowp = O + (size_t)r * ldc + col0;
;                 float sa; if (rowidx) { const int rl = r - cume * BM; sa = (rl < cnte) ? rowmax[u.e * ECAP + rl] : 0.f; } else sa = rowmax[r];
;                 sa *= (1.f / (127.f * 127.f));
;                 float o[8];
; #pragma unroll
;                 for (int n = 0; n < 2; ++n)
; #pragma unroll
;                     for (int j = 0; j < 4; ++j) { const float g = (float)__builtin_bit_cast(i32x4, acc[ai][0][m][n])[j] * (sa * cg[n * 4 + j]), up = (float)__builtin_bit_cast(i32x4, acc[ai][1][m][n])[j] * (sa * cu[n * 4 + j]);
;                         o[n * 4 + j] = g * __builtin_amdgcn_rcpf(1.f + __builtin_amdgcn_exp2f(-1.4426950408889634f * g)) * up; }
;                 u32x2 w; w.x = pack_fp8x4(o[0], o[1], o[2], o[3]); w.y = pack_fp8x4(o[4], o[5], o[6], o[7]);
;                 *(u32x2*)rowp = w; }
	v_cvt_f32_i32_e32 v22, v19
	v_cvt_f32_i32_e32 v19, v24
	v_cvt_f32_i32_e32 v18, v20
	v_cvt_f32_i32_e32 v24, v21
	v_mov_b32_e32 v20, 0
	v_mov_b32_e32 v21, 0
	v_add_u32_e32 v52, 0xa0, v160
	v_mul_f32_e32 v36, 0x38820610, v1
	v_pk_mul_f32 v[38:39], v[122:123], v[36:37] op_sel_hi:[1,0]
	v_pk_mul_f32 v[40:41], v[70:71], v[36:37] op_sel_hi:[1,0]
	v_pk_mul_f32 v[42:43], v[124:125], v[36:37] op_sel_hi:[1,0]
	v_pk_mul_f32 v[46:47], v[126:127], v[36:37] op_sel_hi:[1,0]
	v_pk_mul_f32 v[48:49], v[66:67], v[36:37] op_sel_hi:[1,0]
	v_pk_mul_f32 v[44:45], v[72:73], v[36:37] op_sel_hi:[1,0]
	v_pk_mul_f32 v[50:51], v[128:129], v[36:37] op_sel_hi:[1,0]
	v_pk_mul_f32 v[36:37], v[68:69], v[36:37] op_sel_hi:[1,0]
	v_pk_mul_f32 v[34:35], v[38:39], v[34:35]
	v_pk_mul_f32 v[30:31], v[40:41], v[30:31]
	v_pk_mul_f32 v[26:27], v[42:43], v[26:27]
	v_pk_mul_f32 v[28:29], v[46:47], v[28:29]
	v_pk_mul_f32 v[22:23], v[48:49], v[22:23]
	v_pk_mul_f32 v[18:19], v[50:51], v[18:19]
	v_pk_mul_f32 v[24:25], v[36:37], v[24:25]
	v_mul_f32_e32 v1, 0xbfb8aa3b, v35
	v_mul_f32_e32 v36, 0xbfb8aa3b, v31
	v_mul_f32_e32 v37, 0xbfb8aa3b, v27
	v_mul_f32_e32 v39, 0xbfb8aa3b, v29
	v_mul_f32_e32 v40, 0xbfb8aa3b, v23
	v_mul_f32_e32 v41, 0xbfb8aa3b, v19
	v_mul_f32_e32 v42, 0xbfb8aa3b, v25
	v_exp_f32_e32 v1, v1
	v_exp_f32_e32 v36, v36
	v_exp_f32_e32 v37, v37
	v_exp_f32_e32 v39, v39
	v_exp_f32_e32 v40, v40
	v_exp_f32_e32 v41, v41
	v_exp_f32_e32 v42, v42
	v_pk_mul_f32 v[32:33], v[44:45], v[32:33]
	v_add_f32_e32 v1, 1.0, v1
	v_mul_f32_e32 v38, 0xbfb8aa3b, v33
	v_exp_f32_e32 v38, v38
	v_add_f32_e32 v36, 1.0, v36
	v_add_f32_e32 v37, 1.0, v37
	v_add_f32_e32 v39, 1.0, v39
	v_add_f32_e32 v40, 1.0, v40
	v_add_f32_e32 v41, 1.0, v41
	v_add_f32_e32 v42, 1.0, v42
	v_rcp_f32_e32 v1, v1
	v_rcp_f32_e32 v36, v36
	v_rcp_f32_e32 v37, v37
	v_rcp_f32_e32 v39, v39
	v_rcp_f32_e32 v40, v40
	v_rcp_f32_e32 v41, v41
	v_rcp_f32_e32 v42, v42
	v_add_f32_e32 v38, 1.0, v38
	v_rcp_f32_e32 v38, v38
	v_mul_f32_e32 v1, v35, v1
	v_mul_f32_e32 v31, v31, v36
	v_mul_f32_e32 v27, v27, v37
	v_mul_f32_e32 v29, v29, v39
	v_mul_f32_e32 v23, v23, v40
	v_mul_f32_e32 v19, v19, v41
	v_mul_f32_e32 v25, v25, v42
	v_mul_f32_e32 v1, v34, v1
	v_mul_f32_e32 v30, v30, v31
	v_mul_f32_e32 v26, v26, v27
	v_mul_f32_e32 v28, v28, v29
	v_mul_f32_e32 v22, v22, v23
	v_mul_f32_e32 v18, v18, v19
	v_mul_f32_e32 v19, v24, v25
	v_med3_f32 v1, v1, s54, v170
	v_med3_f32 v23, v30, s54, v170
	v_med3_f32 v24, v26, s54, v170
	v_med3_f32 v26, v28, s54, v170
	v_med3_f32 v22, v22, s54, v170
	v_cvt_pk_fp8_f32 v20, v1, v23
	v_cvt_pk_fp8_f32 v21, v26, v22
	v_mul_f32_e32 v33, v33, v38
	v_mul_f32_e32 v27, v32, v33
	v_med3_f32 v25, v27, s54, v170
	v_med3_f32 v1, v18, s54, v170
	v_med3_f32 v18, v19, s54, v170
	v_cvt_pk_fp8_f32 v20, v24, v25 op_sel:[0,0,1]
	v_cvt_pk_fp8_f32 v21, v1, v18 op_sel:[0,0,1]
	v_mad_i64_i32 v[18:19], s[26:27], v52, s53, v[158:159]
	v_lshl_add_u64 v[18:19], v[18:19], 0, v[156:157]
	global_store_dwordx2 v[18:19], v[20:21], off
	v_mov_b32_e32 v1, v250
	v_cvt_f32_i32_e32 v19, v6
	v_cvt_f32_i32_e32 v18, v14
	v_cvt_f32_i32_e32 v6, v15
	v_cvt_f32_i32_e32 v15, v8
	v_cvt_f32_i32_e32 v14, v16
	v_cvt_f32_i32_e32 v8, v17
	v_cvt_f32_i32_e32 v17, v2
	v_cvt_f32_i32_e32 v16, v10
	v_cvt_f32_i32_e32 v2, v11
	v_cvt_f32_i32_e32 v11, v4
	v_cvt_f32_i32_e32 v4, v13
	v_cvt_f32_i32_e32 v10, v12
	v_mov_b32_e32 v12, 0
	v_mov_b32_e32 v13, 0
	v_add_u32_e32 v36, 0xb0, v160
	v_mul_f32_e32 v20, 0x38820610, v1
	v_pk_mul_f32 v[22:23], v[122:123], v[20:21] op_sel_hi:[1,0]
	v_pk_mul_f32 v[24:25], v[70:71], v[20:21] op_sel_hi:[1,0]
	v_pk_mul_f32 v[26:27], v[124:125], v[20:21] op_sel_hi:[1,0]
	v_pk_mul_f32 v[28:29], v[72:73], v[20:21] op_sel_hi:[1,0]
	v_pk_mul_f32 v[30:31], v[126:127], v[20:21] op_sel_hi:[1,0]
	v_pk_mul_f32 v[32:33], v[66:67], v[20:21] op_sel_hi:[1,0]
	v_pk_mul_f32 v[34:35], v[128:129], v[20:21] op_sel_hi:[1,0]
	v_pk_mul_f32 v[20:21], v[68:69], v[20:21] op_sel_hi:[1,0]
	v_pk_mul_f32 v[18:19], v[22:23], v[18:19]
	v_pk_mul_f32 v[6:7], v[24:25], v[6:7]
	v_pk_mul_f32 v[14:15], v[26:27], v[14:15]
	v_pk_mul_f32 v[8:9], v[28:29], v[8:9]
	v_pk_mul_f32 v[16:17], v[30:31], v[16:17]
	v_pk_mul_f32 v[2:3], v[32:33], v[2:3]
	v_pk_mul_f32 v[4:5], v[20:21], v[4:5]
	v_mul_f32_e32 v1, 0xbfb8aa3b, v19
	v_mul_f32_e32 v20, 0xbfb8aa3b, v7
	v_mul_f32_e32 v21, 0xbfb8aa3b, v15
	v_mul_f32_e32 v22, 0xbfb8aa3b, v9
	v_mul_f32_e32 v23, 0xbfb8aa3b, v17
	v_mul_f32_e32 v24, 0xbfb8aa3b, v3
	v_mul_f32_e32 v26, 0xbfb8aa3b, v5
	v_exp_f32_e32 v1, v1
	v_exp_f32_e32 v20, v20
	v_exp_f32_e32 v21, v21
	v_exp_f32_e32 v22, v22
	v_exp_f32_e32 v23, v23
	v_exp_f32_e32 v24, v24
	v_exp_f32_e32 v26, v26
	v_pk_mul_f32 v[10:11], v[34:35], v[10:11]
	v_add_f32_e32 v1, 1.0, v1
	v_mul_f32_e32 v25, 0xbfb8aa3b, v11
	v_exp_f32_e32 v25, v25
	v_add_f32_e32 v20, 1.0, v20
	v_add_f32_e32 v21, 1.0, v21
	v_add_f32_e32 v22, 1.0, v22
	v_add_f32_e32 v23, 1.0, v23
	v_add_f32_e32 v24, 1.0, v24
	v_add_f32_e32 v26, 1.0, v26
	v_rcp_f32_e32 v1, v1
	v_rcp_f32_e32 v20, v20
	v_rcp_f32_e32 v21, v21
	v_rcp_f32_e32 v22, v22
	v_rcp_f32_e32 v23, v23
	v_rcp_f32_e32 v24, v24
	v_rcp_f32_e32 v26, v26
	v_add_f32_e32 v25, 1.0, v25
	v_rcp_f32_e32 v25, v25
	v_mul_f32_e32 v1, v19, v1
	v_mul_f32_e32 v7, v7, v20
	v_mul_f32_e32 v15, v15, v21
	v_mul_f32_e32 v9, v9, v22
	v_mul_f32_e32 v17, v17, v23
	v_mul_f32_e32 v3, v3, v24
	v_mul_f32_e32 v5, v5, v26
	v_mul_f32_e32 v1, v18, v1
	v_mul_f32_e32 v6, v6, v7
	v_mul_f32_e32 v7, v14, v15
	v_mul_f32_e32 v8, v8, v9
	v_mul_f32_e32 v9, v16, v17
	v_mul_f32_e32 v2, v2, v3
	v_mul_f32_e32 v4, v4, v5
	v_med3_f32 v1, v1, s54, v170
	v_med3_f32 v5, v6, s54, v170
	v_med3_f32 v6, v7, s54, v170
	v_med3_f32 v7, v8, s54, v170
	v_med3_f32 v8, v9, s54, v170
	v_med3_f32 v2, v2, s54, v170
	v_cvt_pk_fp8_f32 v12, v1, v5
	v_cvt_pk_fp8_f32 v13, v8, v2
	v_mul_f32_e32 v11, v11, v25
	v_mul_f32_e32 v3, v10, v11
	v_med3_f32 v1, v3, s54, v170
	v_med3_f32 v2, v4, s54, v170
	v_cvt_pk_fp8_f32 v12, v6, v7 op_sel:[0,0,1]
	v_cvt_pk_fp8_f32 v13, v1, v2 op_sel:[0,0,1]
	v_mad_i64_i32 v[2:3], s[26:27], v36, s53, v[158:159]
	v_lshl_add_u64 v[2:3], v[2:3], 0, v[156:157]
	global_store_dwordx2 v[2:3], v[12:13], off
	s_cbranch_vccnz .LBB0_1150
	s_andn2_b64 vcc, exec, s[8:9]
	s_cbranch_vccnz .LBB0_1149
	s_barrier
	s_branch .LBB0_1149

; __device__ __forceinline__ unsigned cvtpk(float lo, float hi) { f32x2 v = {lo, hi}; bf16x2_t b = __builtin_convertvector(v, bf16x2_t); return __builtin_bit_cast(unsigned, b); }
;     __device__ __forceinline__ void operator()(const f32x4 (&acc)[2][2][4][2], const Unit& u, int wr, int wc, int fr, int fq) const {
;     ...
;         const int row0 = u.pm * BM + wr * 64 + fr, col0 = u.pn * BM + wc * 32 + 8 * fq;
;         const float qsc = (u.pn < 2 || (u.pn >= 14 && u.pn < 18)) ? 0.125f * 1.4426950408889634f : 1.f;
;         f32x4 cmv[2][2], cs[2][2];
; #pragma unroll
;         for (int bj = 0; bj < 2; ++bj)
; #pragma unroll
;             for (int n = 0; n < 2; ++n) { cmv[bj][n] = *(const f32x4*)(colmax + col0 + bj * HALF + 4 * n) * (qsc / (127.f * 127.f)); cs[bj][n] = (f32x4){0.f, 0.f, 0.f, 0.f}; }
; #pragma unroll
;         for (int ai = 0; ai < 2; ++ai)
; #pragma unroll
;             for (int m = 0; m < 4; ++m) { const int r = row0 + ai * HALF + m * 16; bf16_t* rowp = O + (size_t)r * ldc + col0; const float sa = rowmax[r];
; #pragma unroll
;                 for (int bj = 0; bj < 2; ++bj) { f32x4 v[2];
; #pragma unroll
;                     for (int n = 0; n < 2; ++n) { const i32x4_ iv = __builtin_bit_cast(i32x4_, acc[ai][bj][m][n]);
;                         v[n] = (f32x4){(float)iv[0], (float)iv[1], (float)iv[2], (float)iv[3]} * (cmv[bj][n] * sa); cs[bj][n] += v[n]; }
;                     u32x4 w; w.x = cvtpk(v[0][0], v[0][1]); w.y = cvtpk(v[0][2], v[0][3]); w.z = cvtpk(v[1][0], v[1][1]); w.w = cvtpk(v[1][2], v[1][3]);
;                     *(u32x4*)(rowp + bj * HALF) = w; } }
.LBB0_1388:
	s_lshl_b32 s0, s31, 8
	v_or_b32_e32 v170, s0, v173
	v_ashrrev_i32_e32 v171, 31, v170
	v_lshl_add_u64 v[148:149], v[170:171], 2, s[16:17]
	global_load_dwordx4 v[154:157], v[148:149], off
	global_load_dwordx4 v[158:161], v[148:149], off offset:16
	global_load_dwordx4 v[166:169], v[148:149], off offset:528
	global_load_dwordx4 v[162:165], v[148:149], off offset:512
	v_lshl_add_u32 v148, s30, 8, v131
	v_ashrrev_i32_e32 v149, 31, v148
	v_lshl_add_u64 v[152:153], v[148:149], 2, s[14:15]
	global_load_dword v180, v[152:153], off
	global_load_dword v244, v[152:153], off offset:64
	global_load_dword v245, v[152:153], off offset:128
	global_load_dword v246, v[152:153], off offset:192
	global_load_dword v247, v[152:153], off offset:512
	global_load_dword v248, v[152:153], off offset:576
	global_load_dword v249, v[152:153], off offset:640
	global_load_dword v250, v[152:153], off offset:704
	v_mov_b64_e32 v[150:151], s[58:59]
	v_cvt_f32_i32_e32 v187, v117
	v_cvt_f32_i32_e32 v186, v116
	s_cmp_lt_i32 s31, 2
	v_mad_i64_i32 v[116:117], s[34:35], v148, s68, v[150:151]
	s_cselect_b64 s[34:35], -1, 0
	s_add_i32 s23, s31, -14
	s_cmp_lt_u32 s23, 4
	s_cselect_b64 s[36:37], -1, 0
	v_cvt_f32_i32_e32 v129, v129
	v_cvt_f32_i32_e32 v128, v128
	v_cvt_f32_i32_e32 v127, v127
	v_cvt_f32_i32_e32 v126, v126
	v_cvt_f32_i32_e32 v183, v125
	v_cvt_f32_i32_e32 v182, v124
	v_cvt_f32_i32_e32 v123, v123
	v_cvt_f32_i32_e32 v122, v122
	v_lshlrev_b64 v[170:171], 1, v[170:171]
	s_or_b64 vcc, s[34:35], s[36:37]
	v_cvt_f32_i32_e32 v185, v121
	v_cvt_f32_i32_e32 v184, v120
	v_cvt_f32_i32_e32 v119, v119
	v_cvt_f32_i32_e32 v118, v118
	v_cvt_f32_i32_e32 v115, v115
	v_cvt_f32_i32_e32 v114, v114
	v_lshl_add_u64 v[192:193], v[116:117], 0, v[170:171]
	v_cndmask_b32_e32 v116, v177, v178, vcc
	v_or_b32_e32 v188, 16, v148
	v_ashrrev_i32_e32 v189, 31, v188
	v_lshl_add_u64 v[190:191], v[188:189], 2, s[14:15]
	v_add_u32_e32 v1, 0x80, v148
	v_cvt_f32_i32_e32 v7, v7
	v_cvt_f32_i32_e32 v6, v6
	v_cvt_f32_i32_e32 v9, v9
	v_cvt_f32_i32_e32 v8, v8
	v_cvt_f32_i32_e32 v3, v3
	v_cvt_f32_i32_e32 v2, v2
	v_cvt_f32_i32_e32 v5, v5
	v_cvt_f32_i32_e32 v4, v4
	s_and_b32 s23, s31, -2
	s_cmp_lg_u32 s23, 2
	s_waitcnt vmcnt(0)
	v_pk_mul_f32 v[154:155], v[116:117], v[154:155] op_sel_hi:[0,1]
	v_pk_mul_f32 v[156:157], v[116:117], v[156:157] op_sel_hi:[0,1]
	v_pk_mul_f32 v[158:159], v[116:117], v[158:159] op_sel_hi:[0,1]
	v_pk_mul_f32 v[160:161], v[116:117], v[160:161] op_sel_hi:[0,1]
	v_pk_mul_f32 v[162:163], v[116:117], v[162:163] op_sel_hi:[0,1]
	v_pk_mul_f32 v[164:165], v[116:117], v[164:165] op_sel_hi:[0,1]
	v_pk_mul_f32 v[166:167], v[116:117], v[166:167] op_sel_hi:[0,1]
	v_pk_mul_f32 v[168:169], v[116:117], v[168:169] op_sel_hi:[0,1]
	v_pk_mul_f32 v[116:117], v[156:157], v[180:181] op_sel_hi:[1,0]
	v_pk_mul_f32 v[120:121], v[154:155], v[180:181] op_sel_hi:[1,0]
	v_pk_mul_f32 v[196:197], v[160:161], v[180:181] op_sel_hi:[1,0]
	v_pk_mul_f32 v[124:125], v[158:159], v[180:181] op_sel_hi:[1,0]
	v_pk_mul_f32 v[198:199], v[164:165], v[180:181] op_sel_hi:[1,0]
	v_pk_mul_f32 v[200:201], v[162:163], v[180:181] op_sel_hi:[1,0]
	v_pk_mul_f32 v[202:203], v[168:169], v[180:181] op_sel_hi:[1,0]
	v_pk_mul_f32 v[180:181], v[166:167], v[180:181] op_sel_hi:[1,0]
	v_pk_mul_f32 v[126:127], v[120:121], v[126:127]
	v_pk_mul_f32 v[128:129], v[116:117], v[128:129]
	v_pk_mul_f32 v[124:125], v[124:125], v[122:123]
	v_pk_mul_f32 v[122:123], v[196:197], v[182:183]
	v_pk_mul_f32 v[120:121], v[200:201], v[118:119]
	v_pk_mul_f32 v[118:119], v[198:199], v[184:185]
	v_pk_mul_f32 v[116:117], v[180:181], v[114:115]
	v_pk_mul_f32 v[114:115], v[202:203], v[186:187]
	v_cvt_pk_bf16_f32 v180, v126, v127
	v_cvt_pk_bf16_f32 v181, v128, v129
	v_cvt_pk_bf16_f32 v182, v124, v125
	v_cvt_pk_bf16_f32 v183, v122, v123
	v_cvt_pk_bf16_f32 v184, v120, v121
	v_cvt_pk_bf16_f32 v185, v118, v119
	v_cvt_pk_bf16_f32 v186, v116, v117
	v_cvt_pk_bf16_f32 v187, v114, v115
	global_store_dwordx4 v[192:193], v[180:183], off
	global_store_dwordx4 v[192:193], v[184:187], off offset:256
	s_nop 0
	v_mov_b32_e32 v180, v244
	v_cvt_f32_i32_e32 v183, v111
	v_cvt_f32_i32_e32 v182, v110
	v_cvt_f32_i32_e32 v111, v113
	v_cvt_f32_i32_e32 v110, v112
	v_cvt_f32_i32_e32 v185, v107
	v_cvt_f32_i32_e32 v184, v106
	v_cvt_f32_i32_e32 v107, v109
	v_cvt_f32_i32_e32 v106, v108
	v_cvt_f32_i32_e32 v187, v103
	v_cvt_f32_i32_e32 v186, v102
	v_cvt_f32_i32_e32 v103, v105
	v_cvt_f32_i32_e32 v102, v104
	v_cvt_f32_i32_e32 v191, v99
	v_cvt_f32_i32_e32 v190, v98
	v_cvt_f32_i32_e32 v99, v101
	v_cvt_f32_i32_e32 v98, v100
	v_mad_i64_i32 v[100:101], s[34:35], v188, s68, v[150:151]
	v_lshl_add_u64 v[196:197], v[100:101], 0, v[170:171]
	v_or_b32_e32 v192, 32, v148
	v_ashrrev_i32_e32 v193, 31, v192
	v_lshl_add_u64 v[188:189], v[192:193], 2, s[14:15]
	v_pk_mul_f32 v[100:101], v[154:155], v[180:181] op_sel_hi:[1,0]
	v_pk_mul_f32 v[104:105], v[156:157], v[180:181] op_sel_hi:[1,0]
	v_pk_mul_f32 v[108:109], v[158:159], v[180:181] op_sel_hi:[1,0]
	v_pk_mul_f32 v[198:199], v[160:161], v[180:181] op_sel_hi:[1,0]
	v_pk_mul_f32 v[200:201], v[162:163], v[180:181] op_sel_hi:[1,0]
	v_pk_mul_f32 v[202:203], v[164:165], v[180:181] op_sel_hi:[1,0]
	v_pk_mul_f32 v[204:205], v[166:167], v[180:181] op_sel_hi:[1,0]
	v_pk_mul_f32 v[180:181], v[168:169], v[180:181] op_sel_hi:[1,0]
	v_pk_mul_f32 v[110:111], v[104:105], v[110:111]
	v_pk_mul_f32 v[112:113], v[100:101], v[182:183]
	v_pk_mul_f32 v[106:107], v[198:199], v[106:107]
	v_pk_mul_f32 v[108:109], v[108:109], v[184:185]
	v_pk_mul_f32 v[102:103], v[202:203], v[102:103]
	v_pk_mul_f32 v[104:105], v[200:201], v[186:187]
	v_pk_mul_f32 v[98:99], v[180:181], v[98:99]
; __device__ __forceinline__ unsigned cvtpk(float lo, float hi) { f32x2 v = {lo, hi}; bf16x2_t b = __builtin_convertvector(v, bf16x2_t); return __builtin_bit_cast(unsigned, b); }
;     __device__ __forceinline__ void operator()(const f32x4 (&acc)[2][2][4][2], const Unit& u, int wr, int wc, int fr, int fq) const {
;     ...
;             for (int m = 0; m < 4; ++m) { const int r = row0 + ai * HALF + m * 16; bf16_t* rowp = O + (size_t)r * ldc + col0; const float sa = rowmax[r];
; #pragma unroll
;                 for (int bj = 0; bj < 2; ++bj) { f32x4 v[2];
; #pragma unroll
;                     for (int n = 0; n < 2; ++n) { const i32x4_ iv = __builtin_bit_cast(i32x4_, acc[ai][bj][m][n]);
;                         v[n] = (f32x4){(float)iv[0], (float)iv[1], (float)iv[2], (float)iv[3]} * (cmv[bj][n] * sa); cs[bj][n] += v[n]; }
;                     u32x4 w; w.x = cvtpk(v[0][0], v[0][1]); w.y = cvtpk(v[0][2], v[0][3]); w.z = cvtpk(v[1][0], v[1][1]); w.w = cvtpk(v[1][2], v[1][3]);
;                     *(u32x4*)(rowp + bj * HALF) = w; } }
	v_pk_mul_f32 v[100:101], v[204:205], v[190:191]
	v_cvt_pk_bf16_f32 v180, v112, v113
	v_cvt_pk_bf16_f32 v181, v110, v111
	v_cvt_pk_bf16_f32 v182, v108, v109
	v_cvt_pk_bf16_f32 v183, v106, v107
	v_cvt_pk_bf16_f32 v184, v104, v105
	v_cvt_pk_bf16_f32 v185, v102, v103
	v_cvt_pk_bf16_f32 v186, v100, v101
	v_cvt_pk_bf16_f32 v187, v98, v99
	global_store_dwordx4 v[196:197], v[180:183], off
	global_store_dwordx4 v[196:197], v[184:187], off offset:256
	s_nop 0
	v_mov_b32_e32 v180, v245
	v_cvt_f32_i32_e32 v183, v95
	v_cvt_f32_i32_e32 v182, v94
	v_cvt_f32_i32_e32 v95, v97
	v_cvt_f32_i32_e32 v94, v96
	v_cvt_f32_i32_e32 v185, v91
	v_cvt_f32_i32_e32 v184, v90
	v_cvt_f32_i32_e32 v91, v93
	v_cvt_f32_i32_e32 v90, v92
	v_cvt_f32_i32_e32 v187, v87
	v_cvt_f32_i32_e32 v186, v86
	v_cvt_f32_i32_e32 v87, v89
	v_cvt_f32_i32_e32 v86, v88
	v_cvt_f32_i32_e32 v189, v83
	v_cvt_f32_i32_e32 v188, v82
	v_cvt_f32_i32_e32 v83, v85
	v_cvt_f32_i32_e32 v82, v84
	v_mad_i64_i32 v[84:85], s[34:35], v192, s68, v[150:151]
	v_lshl_add_u64 v[196:197], v[84:85], 0, v[170:171]
	v_or_b32_e32 v190, 48, v148
	v_ashrrev_i32_e32 v191, 31, v190
	v_lshl_add_u64 v[192:193], v[190:191], 2, s[14:15]
	v_pk_mul_f32 v[84:85], v[154:155], v[180:181] op_sel_hi:[1,0]
	v_pk_mul_f32 v[88:89], v[156:157], v[180:181] op_sel_hi:[1,0]
	v_pk_mul_f32 v[92:93], v[158:159], v[180:181] op_sel_hi:[1,0]
	v_pk_mul_f32 v[198:199], v[160:161], v[180:181] op_sel_hi:[1,0]
	v_pk_mul_f32 v[200:201], v[162:163], v[180:181] op_sel_hi:[1,0]
	v_pk_mul_f32 v[202:203], v[164:165], v[180:181] op_sel_hi:[1,0]
	v_pk_mul_f32 v[204:205], v[166:167], v[180:181] op_sel_hi:[1,0]
	v_pk_mul_f32 v[180:181], v[168:169], v[180:181] op_sel_hi:[1,0]
	v_pk_mul_f32 v[94:95], v[88:89], v[94:95]
	v_pk_mul_f32 v[96:97], v[84:85], v[182:183]
	v_pk_mul_f32 v[90:91], v[198:199], v[90:91]
	v_pk_mul_f32 v[92:93], v[92:93], v[184:185]
	v_pk_mul_f32 v[86:87], v[202:203], v[86:87]
	v_pk_mul_f32 v[88:89], v[200:201], v[186:187]
	v_pk_mul_f32 v[82:83], v[180:181], v[82:83]
	v_pk_mul_f32 v[84:85], v[204:205], v[188:189]
	v_cvt_pk_bf16_f32 v180, v96, v97
	v_cvt_pk_bf16_f32 v181, v94, v95
	v_cvt_pk_bf16_f32 v182, v92, v93
	v_cvt_pk_bf16_f32 v183, v90, v91
	v_cvt_pk_bf16_f32 v184, v88, v89
	v_cvt_pk_bf16_f32 v185, v86, v87
	v_cvt_pk_bf16_f32 v186, v84, v85
	v_cvt_pk_bf16_f32 v187, v82, v83
	global_store_dwordx4 v[196:197], v[180:183], off
	global_store_dwordx4 v[196:197], v[184:187], off offset:256
	s_nop 0
	v_mov_b32_e32 v180, v246
	v_cvt_f32_i32_e32 v183, v79
	v_cvt_f32_i32_e32 v182, v78
	v_cvt_f32_i32_e32 v79, v81
	v_cvt_f32_i32_e32 v78, v80
	v_cvt_f32_i32_e32 v185, v75
	v_cvt_f32_i32_e32 v184, v74
	v_cvt_f32_i32_e32 v75, v77
	v_cvt_f32_i32_e32 v74, v76
	v_cvt_f32_i32_e32 v187, v71
	v_cvt_f32_i32_e32 v186, v70
	v_cvt_f32_i32_e32 v71, v73
	v_cvt_f32_i32_e32 v70, v72
	v_cvt_f32_i32_e32 v189, v67
	v_cvt_f32_i32_e32 v188, v66
	v_cvt_f32_i32_e32 v67, v69
	v_cvt_f32_i32_e32 v66, v68
	v_mad_i64_i32 v[68:69], s[34:35], v190, s68, v[150:151]
	v_lshl_add_u64 v[190:191], v[68:69], 0, v[170:171]
	v_pk_mul_f32 v[68:69], v[154:155], v[180:181] op_sel_hi:[1,0]
	v_pk_mul_f32 v[72:73], v[156:157], v[180:181] op_sel_hi:[1,0]
	v_pk_mul_f32 v[76:77], v[158:159], v[180:181] op_sel_hi:[1,0]
	v_pk_mul_f32 v[192:193], v[160:161], v[180:181] op_sel_hi:[1,0]
	v_pk_mul_f32 v[196:197], v[162:163], v[180:181] op_sel_hi:[1,0]
	v_pk_mul_f32 v[198:199], v[164:165], v[180:181] op_sel_hi:[1,0]
	v_pk_mul_f32 v[200:201], v[166:167], v[180:181] op_sel_hi:[1,0]
	v_pk_mul_f32 v[180:181], v[168:169], v[180:181] op_sel_hi:[1,0]
	v_pk_mul_f32 v[78:79], v[72:73], v[78:79]
	v_pk_mul_f32 v[80:81], v[68:69], v[182:183]
	v_pk_mul_f32 v[74:75], v[192:193], v[74:75]
	v_pk_mul_f32 v[76:77], v[76:77], v[184:185]
	v_pk_mul_f32 v[70:71], v[198:199], v[70:71]
	v_pk_mul_f32 v[72:73], v[196:197], v[186:187]
	v_pk_mul_f32 v[66:67], v[180:181], v[66:67]
	v_pk_mul_f32 v[68:69], v[200:201], v[188:189]
	v_cvt_pk_bf16_f32 v180, v80, v81
	v_cvt_pk_bf16_f32 v181, v78, v79
	v_cvt_pk_bf16_f32 v182, v76, v77
	v_cvt_pk_bf16_f32 v183, v74, v75
	v_cvt_pk_bf16_f32 v184, v72, v73
	v_cvt_pk_bf16_f32 v185, v70, v71
	v_cvt_pk_bf16_f32 v186, v68, v69
	v_cvt_pk_bf16_f32 v187, v66, v67
	global_store_dwordx4 v[190:191], v[180:183], off
	global_store_dwordx4 v[190:191], v[184:187], off offset:256
	s_nop 0
	v_mov_b32_e32 v180, v247
	v_cvt_f32_i32_e32 v183, v63
	v_cvt_f32_i32_e32 v182, v62
	v_cvt_f32_i32_e32 v63, v65
	v_cvt_f32_i32_e32 v62, v64
	v_cvt_f32_i32_e32 v185, v59
	v_cvt_f32_i32_e32 v184, v58
	v_cvt_f32_i32_e32 v59, v61
	v_cvt_f32_i32_e32 v58, v60
	v_cvt_f32_i32_e32 v187, v55
	v_cvt_f32_i32_e32 v186, v54
	v_cvt_f32_i32_e32 v55, v57
	v_cvt_f32_i32_e32 v54, v56
	v_cvt_f32_i32_e32 v189, v51
	v_cvt_f32_i32_e32 v188, v50
	v_cvt_f32_i32_e32 v51, v53
	v_cvt_f32_i32_e32 v50, v52
	v_mad_i64_i32 v[52:53], s[34:35], v1, s68, v[150:151]
	v_lshl_add_u64 v[190:191], v[52:53], 0, v[170:171]
	v_add_u32_e32 v1, 0x90, v148
	v_pk_mul_f32 v[52:53], v[154:155], v[180:181] op_sel_hi:[1,0]
	v_pk_mul_f32 v[56:57], v[156:157], v[180:181] op_sel_hi:[1,0]
	v_pk_mul_f32 v[60:61], v[158:159], v[180:181] op_sel_hi:[1,0]
	v_pk_mul_f32 v[192:193], v[160:161], v[180:181] op_sel_hi:[1,0]
	v_pk_mul_f32 v[196:197], v[162:163], v[180:181] op_sel_hi:[1,0]
	v_pk_mul_f32 v[198:199], v[164:165], v[180:181] op_sel_hi:[1,0]
	v_pk_mul_f32 v[200:201], v[166:167], v[180:181] op_sel_hi:[1,0]
	v_pk_mul_f32 v[180:181], v[168:169], v[180:181] op_sel_hi:[1,0]
	v_pk_mul_f32 v[62:63], v[56:57], v[62:63]
	v_pk_mul_f32 v[64:65], v[52:53], v[182:183]
	v_pk_mul_f32 v[58:59], v[192:193], v[58:59]
	v_pk_mul_f32 v[60:61], v[60:61], v[184:185]
	v_pk_mul_f32 v[54:55], v[198:199], v[54:55]
; __device__ __forceinline__ unsigned cvtpk(float lo, float hi) { f32x2 v = {lo, hi}; bf16x2_t b = __builtin_convertvector(v, bf16x2_t); return __builtin_bit_cast(unsigned, b); }
;     __device__ __forceinline__ void operator()(const f32x4 (&acc)[2][2][4][2], const Unit& u, int wr, int wc, int fr, int fq) const {
;     ...
;             for (int m = 0; m < 4; ++m) { const int r = row0 + ai * HALF + m * 16; bf16_t* rowp = O + (size_t)r * ldc + col0; const float sa = rowmax[r];
; #pragma unroll
;                 for (int bj = 0; bj < 2; ++bj) { f32x4 v[2];
; #pragma unroll
;                     for (int n = 0; n < 2; ++n) { const i32x4_ iv = __builtin_bit_cast(i32x4_, acc[ai][bj][m][n]);
;                         v[n] = (f32x4){(float)iv[0], (float)iv[1], (float)iv[2], (float)iv[3]} * (cmv[bj][n] * sa); cs[bj][n] += v[n]; }
;                     u32x4 w; w.x = cvtpk(v[0][0], v[0][1]); w.y = cvtpk(v[0][2], v[0][3]); w.z = cvtpk(v[1][0], v[1][1]); w.w = cvtpk(v[1][2], v[1][3]);
;                     *(u32x4*)(rowp + bj * HALF) = w; } }
	v_pk_mul_f32 v[56:57], v[196:197], v[186:187]
	v_pk_mul_f32 v[50:51], v[180:181], v[50:51]
	v_pk_mul_f32 v[52:53], v[200:201], v[188:189]
	v_cvt_pk_bf16_f32 v180, v64, v65
	v_cvt_pk_bf16_f32 v181, v62, v63
	v_cvt_pk_bf16_f32 v182, v60, v61
	v_cvt_pk_bf16_f32 v183, v58, v59
	v_cvt_pk_bf16_f32 v184, v56, v57
	v_cvt_pk_bf16_f32 v185, v54, v55
	v_cvt_pk_bf16_f32 v186, v52, v53
	v_cvt_pk_bf16_f32 v187, v50, v51
	global_store_dwordx4 v[190:191], v[180:183], off
	global_store_dwordx4 v[190:191], v[184:187], off offset:256
	s_nop 0
	v_mov_b32_e32 v180, v248
	v_cvt_f32_i32_e32 v183, v47
	v_cvt_f32_i32_e32 v182, v46
	v_cvt_f32_i32_e32 v47, v49
	v_cvt_f32_i32_e32 v46, v48
	v_cvt_f32_i32_e32 v185, v43
	v_cvt_f32_i32_e32 v184, v42
	v_cvt_f32_i32_e32 v43, v45
	v_cvt_f32_i32_e32 v42, v44
	v_cvt_f32_i32_e32 v187, v39
	v_cvt_f32_i32_e32 v186, v38
	v_cvt_f32_i32_e32 v39, v41
	v_cvt_f32_i32_e32 v38, v40
	v_cvt_f32_i32_e32 v189, v35
	v_cvt_f32_i32_e32 v188, v34
	v_cvt_f32_i32_e32 v35, v37
	v_cvt_f32_i32_e32 v34, v36
	v_mad_i64_i32 v[36:37], s[34:35], v1, s68, v[150:151]
	v_lshl_add_u64 v[190:191], v[36:37], 0, v[170:171]
	v_add_u32_e32 v1, 0xa0, v148
	v_pk_mul_f32 v[36:37], v[154:155], v[180:181] op_sel_hi:[1,0]
	v_pk_mul_f32 v[40:41], v[156:157], v[180:181] op_sel_hi:[1,0]
	v_pk_mul_f32 v[44:45], v[158:159], v[180:181] op_sel_hi:[1,0]
	v_pk_mul_f32 v[192:193], v[160:161], v[180:181] op_sel_hi:[1,0]
	v_pk_mul_f32 v[196:197], v[162:163], v[180:181] op_sel_hi:[1,0]
	v_pk_mul_f32 v[198:199], v[164:165], v[180:181] op_sel_hi:[1,0]
	v_pk_mul_f32 v[200:201], v[166:167], v[180:181] op_sel_hi:[1,0]
	v_pk_mul_f32 v[180:181], v[168:169], v[180:181] op_sel_hi:[1,0]
	v_pk_mul_f32 v[46:47], v[40:41], v[46:47]
	v_pk_mul_f32 v[48:49], v[36:37], v[182:183]
	v_pk_mul_f32 v[42:43], v[192:193], v[42:43]
	v_pk_mul_f32 v[44:45], v[44:45], v[184:185]
	v_pk_mul_f32 v[38:39], v[198:199], v[38:39]
	v_pk_mul_f32 v[40:41], v[196:197], v[186:187]
	v_pk_mul_f32 v[34:35], v[180:181], v[34:35]
	v_pk_mul_f32 v[36:37], v[200:201], v[188:189]
	v_cvt_pk_bf16_f32 v180, v48, v49
	v_cvt_pk_bf16_f32 v181, v46, v47
	v_cvt_pk_bf16_f32 v182, v44, v45
	v_cvt_pk_bf16_f32 v183, v42, v43
	v_cvt_pk_bf16_f32 v184, v40, v41
	v_cvt_pk_bf16_f32 v185, v38, v39
	v_cvt_pk_bf16_f32 v186, v36, v37
	v_cvt_pk_bf16_f32 v187, v34, v35
	global_store_dwordx4 v[190:191], v[180:183], off
	global_store_dwordx4 v[190:191], v[184:187], off offset:256
	s_nop 0
	v_mov_b32_e32 v180, v249
	v_cvt_f32_i32_e32 v183, v31
	v_cvt_f32_i32_e32 v182, v30
	v_cvt_f32_i32_e32 v31, v33
	v_cvt_f32_i32_e32 v30, v32
	v_cvt_f32_i32_e32 v185, v27
	v_cvt_f32_i32_e32 v184, v26
	v_cvt_f32_i32_e32 v27, v29
	v_cvt_f32_i32_e32 v26, v28
	v_cvt_f32_i32_e32 v187, v15
	v_cvt_f32_i32_e32 v186, v14
	v_cvt_f32_i32_e32 v15, v17
	v_cvt_f32_i32_e32 v14, v16
	v_cvt_f32_i32_e32 v189, v11
	v_cvt_f32_i32_e32 v188, v10
	v_cvt_f32_i32_e32 v11, v13
	v_cvt_f32_i32_e32 v10, v12
	v_mad_i64_i32 v[12:13], s[34:35], v1, s68, v[150:151]
	v_lshl_add_u64 v[190:191], v[12:13], 0, v[170:171]
	v_add_u32_e32 v1, 0xb0, v148
	v_pk_mul_f32 v[12:13], v[154:155], v[180:181] op_sel_hi:[1,0]
	v_pk_mul_f32 v[16:17], v[156:157], v[180:181] op_sel_hi:[1,0]
	v_pk_mul_f32 v[28:29], v[158:159], v[180:181] op_sel_hi:[1,0]
	v_pk_mul_f32 v[192:193], v[160:161], v[180:181] op_sel_hi:[1,0]
	v_pk_mul_f32 v[196:197], v[162:163], v[180:181] op_sel_hi:[1,0]
	v_pk_mul_f32 v[198:199], v[164:165], v[180:181] op_sel_hi:[1,0]
	v_pk_mul_f32 v[200:201], v[166:167], v[180:181] op_sel_hi:[1,0]
	v_pk_mul_f32 v[180:181], v[168:169], v[180:181] op_sel_hi:[1,0]
	v_pk_mul_f32 v[30:31], v[16:17], v[30:31]
	v_pk_mul_f32 v[32:33], v[12:13], v[182:183]
	v_pk_mul_f32 v[26:27], v[192:193], v[26:27]
	v_pk_mul_f32 v[28:29], v[28:29], v[184:185]
	v_pk_mul_f32 v[14:15], v[198:199], v[14:15]
	v_pk_mul_f32 v[16:17], v[196:197], v[186:187]
	v_pk_mul_f32 v[10:11], v[180:181], v[10:11]
	v_pk_mul_f32 v[12:13], v[200:201], v[188:189]
	v_cvt_pk_bf16_f32 v180, v32, v33
	v_cvt_pk_bf16_f32 v181, v30, v31
	v_cvt_pk_bf16_f32 v182, v28, v29
	v_cvt_pk_bf16_f32 v183, v26, v27
	v_cvt_pk_bf16_f32 v184, v16, v17
	v_cvt_pk_bf16_f32 v185, v14, v15
	v_cvt_pk_bf16_f32 v186, v12, v13
	v_cvt_pk_bf16_f32 v187, v10, v11
	global_store_dwordx4 v[190:191], v[180:183], off
	global_store_dwordx4 v[190:191], v[184:187], off offset:256
	s_nop 0
	v_mov_b32_e32 v152, v250
	v_cvt_f32_i32_e32 v181, v23
	v_cvt_f32_i32_e32 v180, v22
	v_cvt_f32_i32_e32 v183, v25
	v_cvt_f32_i32_e32 v182, v24
	v_cvt_f32_i32_e32 v185, v19
	v_cvt_f32_i32_e32 v184, v18
	v_cvt_f32_i32_e32 v187, v21
	v_cvt_f32_i32_e32 v186, v20
	v_mad_i64_i32 v[18:19], s[34:35], v1, s68, v[150:151]
	v_lshl_add_u64 v[170:171], v[18:19], 0, v[170:171]
	v_pk_mul_f32 v[18:19], v[154:155], v[152:153] op_sel_hi:[1,0]
	v_pk_mul_f32 v[20:21], v[156:157], v[152:153] op_sel_hi:[1,0]
	v_pk_mul_f32 v[148:149], v[158:159], v[152:153] op_sel_hi:[1,0]
	v_pk_mul_f32 v[150:151], v[160:161], v[152:153] op_sel_hi:[1,0]
	v_pk_mul_f32 v[154:155], v[162:163], v[152:153] op_sel_hi:[1,0]
	v_pk_mul_f32 v[156:157], v[164:165], v[152:153] op_sel_hi:[1,0]
	v_pk_mul_f32 v[158:159], v[166:167], v[152:153] op_sel_hi:[1,0]
	v_pk_mul_f32 v[152:153], v[168:169], v[152:153] op_sel_hi:[1,0]
	v_pk_mul_f32 v[22:23], v[20:21], v[8:9]
	v_pk_mul_f32 v[24:25], v[18:19], v[6:7]
	v_pk_mul_f32 v[18:19], v[150:151], v[4:5]
	v_pk_mul_f32 v[20:21], v[148:149], v[2:3]
	v_pk_mul_f32 v[6:7], v[156:157], v[182:183]
	v_pk_mul_f32 v[8:9], v[154:155], v[180:181]
	v_pk_mul_f32 v[2:3], v[152:153], v[186:187]
	v_pk_mul_f32 v[4:5], v[158:159], v[184:185]
	v_cvt_pk_bf16_f32 v148, v24, v25
	v_cvt_pk_bf16_f32 v149, v22, v23
	v_cvt_pk_bf16_f32 v150, v20, v21
	v_cvt_pk_bf16_f32 v151, v18, v19
	v_cvt_pk_bf16_f32 v152, v8, v9
	v_cvt_pk_bf16_f32 v153, v6, v7
	v_cvt_pk_bf16_f32 v154, v4, v5
	v_cvt_pk_bf16_f32 v155, v2, v3
	global_store_dwordx4 v[170:171], v[148:151], off
	global_store_dwordx4 v[170:171], v[152:155], off offset:256
	s_cbranch_scc1 .LBB0_1398
; __device__ __forceinline__ unsigned cvtpk(float lo, float hi) { f32x2 v = {lo, hi}; bf16x2_t b = __builtin_convertvector(v, bf16x2_t); return __builtin_bit_cast(unsigned, b); }
;     __device__ __forceinline__ void operator()(const f32x4 (&acc)[2][2][4][2], const Unit& u, int wr, int wc, int fr, int fq) const {
;     ...
;                         v[n] = (f32x4){(float)iv[0], (float)iv[1], (float)iv[2], (float)iv[3]} * (cmv[bj][n] * sa); cs[bj][n] += v[n]; }
;                     u32x4 w; w.x = cvtpk(v[0][0], v[0][1]); w.y = cvtpk(v[0][2], v[0][3]); w.z = cvtpk(v[1][0], v[1][1]); w.w = cvtpk(v[1][2], v[1][3]);
;                     *(u32x4*)(rowp + bj * HALF) = w; } }
;         if (u.pn == 2 || u.pn == 3) {
; #pragma unroll
;             for (int bj = 0; bj < 2; ++bj)
; #pragma unroll
;                 for (int n = 0; n < 2; ++n) {
; #pragma unroll
;                     for (int j = 0; j < 4; ++j) { float v = cs[bj][n][j]; v += __shfl_xor(v, 1); v += __shfl_xor(v, 2); v += __shfl_xor(v, 4); v += __shfl_xor(v, 8); cs[bj][n][j] = v; }
;                     if (fr == 0) { float* kp = kmean + (size_t)u.pm * 512 + (u.pn - 2) * BM + bj * HALF + wc * 32 + 8 * fq + 4 * n;
; #pragma unroll
;                         for (int j = 0; j < 4; ++j) atomicAdd(kp + j, cs[bj][n][j] * (1.f / 256.f)); } }
	v_pk_add_f32 v[128:129], v[128:129], 0 op_sel_hi:[1,0]
	v_pk_add_f32 v[126:127], v[126:127], 0 op_sel_hi:[1,0]
	v_pk_add_f32 v[110:111], v[128:129], v[110:111]
	v_pk_add_f32 v[112:113], v[126:127], v[112:113]
	v_pk_add_f32 v[94:95], v[110:111], v[94:95]
	v_pk_add_f32 v[96:97], v[112:113], v[96:97]
	v_pk_add_f32 v[78:79], v[94:95], v[78:79]
	v_pk_add_f32 v[80:81], v[96:97], v[80:81]
	v_pk_add_f32 v[62:63], v[78:79], v[62:63]
	v_pk_add_f32 v[64:65], v[80:81], v[64:65]
	v_pk_add_f32 v[46:47], v[62:63], v[46:47]
	v_xor_b32_e32 v1, 1, v179
	v_pk_add_f32 v[30:31], v[46:47], v[30:31]
	v_pk_add_f32 v[48:49], v[64:65], v[48:49]
	v_pk_add_f32 v[46:47], v[30:31], v[22:23]
	v_and_b32_e32 v22, 64, v179
	v_add_u32_e32 v30, 64, v22
	v_cmp_lt_i32_e32 vcc, v1, v30
	v_pk_add_f32 v[32:33], v[48:49], v[32:33]
	v_xor_b32_e32 v22, 2, v179
	v_cndmask_b32_e32 v1, v179, v1, vcc
	v_pk_add_f32 v[24:25], v[32:33], v[24:25]
	v_lshlrev_b32_e32 v1, 2, v1
	ds_bpermute_b32 v23, v1, v24
	v_cmp_lt_i32_e32 vcc, v22, v30
	v_xor_b32_e32 v31, 4, v179
	ds_bpermute_b32 v48, v1, v25
	v_cndmask_b32_e32 v22, v179, v22, vcc
	v_lshlrev_b32_e32 v22, 2, v22
	s_waitcnt lgkmcnt(1)
	v_add_f32_e32 v24, v24, v23
	ds_bpermute_b32 v32, v22, v24
	v_cmp_lt_i32_e32 vcc, v31, v30
	s_waitcnt lgkmcnt(1)
	v_add_f32_e32 v25, v25, v48
	ds_bpermute_b32 v48, v22, v25
	v_cndmask_b32_e32 v23, v179, v31, vcc
	v_lshlrev_b32_e32 v23, 2, v23
	s_waitcnt lgkmcnt(1)
	v_add_f32_e32 v32, v24, v32
	ds_bpermute_b32 v33, v23, v32
	v_xor_b32_e32 v31, 8, v179
	v_cmp_lt_i32_e32 vcc, v31, v30
	s_waitcnt lgkmcnt(1)
	v_add_f32_e32 v25, v25, v48
	ds_bpermute_b32 v48, v23, v25
	s_waitcnt lgkmcnt(1)
	v_add_f32_e32 v30, v32, v33
	ds_bpermute_b32 v32, v1, v46
	ds_bpermute_b32 v33, v1, v47
	v_cndmask_b32_e32 v24, v179, v31, vcc
	v_lshlrev_b32_e32 v24, 2, v24
	ds_bpermute_b32 v31, v24, v30
	s_waitcnt lgkmcnt(2)
	v_add_f32_e32 v32, v46, v32
	s_waitcnt lgkmcnt(1)
	v_add_f32_e32 v33, v47, v33
	ds_bpermute_b32 v46, v22, v32
	ds_bpermute_b32 v47, v22, v33
	s_ashr_i32 s31, s30, 31
	s_lshl_b64 s[30:31], s[30:31], 11
	s_waitcnt lgkmcnt(1)
	v_add_f32_e32 v46, v32, v46
	s_waitcnt lgkmcnt(0)
	v_add_f32_e32 v62, v33, v47
	ds_bpermute_b32 v49, v23, v46
	ds_bpermute_b32 v63, v23, v62
	v_add_f32_e32 v32, v25, v48
	ds_bpermute_b32 v33, v24, v32
	v_lshlrev_b32_e32 v25, 2, v130
	s_waitcnt lgkmcnt(2)
	v_add_f32_e32 v46, v46, v49
	s_waitcnt lgkmcnt(1)
	v_add_f32_e32 v48, v62, v63
	ds_bpermute_b32 v47, v24, v46
	ds_bpermute_b32 v49, v24, v48
	s_and_saveexec_b64 s[34:35], s[6:7]
	s_cbranch_execz .LBB0_1391
	s_add_u32 s23, s54, s30
	s_addc_u32 s25, s55, s31
	s_lshl_b64 s[36:37], s[0:1], 2
	s_add_u32 s23, s23, s36
	s_addc_u32 s25, s25, s37
	s_lshl_b32 s36, s56, 2
	v_add_f32_e32 v30, v30, v31
	s_add_u32 s36, s23, s36
	s_waitcnt lgkmcnt(2)
	v_add_f32_e32 v31, v32, v33
	s_addc_u32 s37, s25, 0
	v_mul_f32_e32 v30, 0x3b800000, v30
	s_waitcnt lgkmcnt(1)
	v_add_f32_e32 v32, v46, v47
	global_atomic_add_f32 v25, v30, s[36:37] offset:-2048
	v_mul_f32_e32 v30, 0x3b800000, v31
	s_waitcnt lgkmcnt(0)
	v_add_f32_e32 v48, v48, v49
	global_atomic_add_f32 v25, v30, s[36:37] offset:-2044
	v_mul_f32_e32 v30, 0x3b800000, v32
	global_atomic_add_f32 v25, v30, s[36:37] offset:-2040
	v_mul_f32_e32 v30, 0x3b800000, v48
	global_atomic_add_f32 v25, v30, s[36:37] offset:-2036
